# nt on the retention epilogue gate (g) loads, both retention variants
# baseline (speedup 1.0000x reference)
.LBB0_513:
	s_or_b64 exec, exec, s[0:1]
	v_and_or_b32 v140, v128, 15, s8
	v_ashrrev_i32_e32 v128, 1, v128
	v_and_b32_e32 v128, -8, v128
	s_add_i32 s0, 0, 0x22100
	v_add_u32_e32 v132, s36, v128
	v_lshl_add_u32 v128, v140, 4, s0
	s_waitcnt lgkmcnt(0)
	s_barrier
	s_waitcnt lgkmcnt(0)
	ds_read_b128 v[128:131], v128
	s_or_b32 s20, s16, s20
	s_mov_b32 s21, s17
	v_ashrrev_i32_e32 v141, 31, v140
	v_ashrrev_i32_e32 v133, 31, v132
	s_waitcnt lgkmcnt(0)
	v_mov_b32_e32 v134, v129
	v_mov_b32_e32 v135, v130
	v_mov_b32_e32 v129, v131
	v_pk_add_f32 v[128:129], v[134:135], v[128:129]
	v_lshlrev_b64 v[138:139], 1, v[132:133]
	v_add_f32_e32 v128, v128, v129
	v_fmamk_f32 v128, v128, 0x3b000000, v189
	v_rsq_f32_e32 v146, v128
	v_lshl_add_u64 v[128:129], s[20:21], 0, v[140:141]
	v_lshlrev_b64 v[128:129], 13, v[128:129]
	v_lshl_add_u64 v[130:131], s[66:67], 0, v[128:129]
	v_lshl_add_u64 v[142:143], v[130:131], 0, v[138:139]
	global_load_dwordx4 v[148:151], v[142:143], off nt
	v_lshl_add_u64 v[136:137], v[132:133], 2, s[70:71]
	v_lshl_add_u64 v[144:145], s[34:35], 0, v[128:129]
	global_load_dwordx4 v[128:131], v[136:137], off offset:16
	global_load_dwordx4 v[132:135], v[136:137], off
	v_mul_f32_e32 v120, v120, v146
	v_mul_f32_e32 v121, v121, v146
	v_mul_f32_e32 v122, v122, v146
	v_mul_f32_e32 v124, v124, v146
	v_mul_f32_e32 v123, v123, v146
	v_mul_f32_e32 v112, v112, v146
	v_mul_f32_e32 v113, v113, v146
	v_mul_f32_e32 v114, v114, v146
	v_mul_f32_e32 v116, v116, v146
	v_mul_f32_e32 v115, v115, v146
	v_mul_f32_e32 v104, v104, v146
	v_mul_f32_e32 v105, v105, v146
	v_mul_f32_e32 v106, v106, v146
	v_mul_f32_e32 v108, v108, v146
	v_mul_f32_e32 v107, v107, v146
	v_mul_f32_e32 v96, v96, v146
	v_mul_f32_e32 v97, v97, v146
	v_mul_f32_e32 v98, v98, v146
	v_mul_f32_e32 v100, v100, v146
	v_mul_f32_e32 v99, v99, v146
	s_and_b64 vcc, exec, s[18:19]
	s_waitcnt vmcnt(2)
	v_lshlrev_b32_e32 v152, 16, v150
	v_and_b32_e32 v147, 0xffff0000, v148
	s_waitcnt vmcnt(1)
	v_mul_f32_e32 v120, v128, v120
	v_mul_f32_e32 v128, 0xbfb8aa3b, v152
	v_exp_f32_e32 v128, v128
	v_mul_f32_e32 v120, v120, v152
	v_and_b32_e32 v150, 0xffff0000, v150
	v_mul_f32_e32 v121, v129, v121
	v_add_f32_e32 v128, 1.0, v128
	v_rcp_f32_e32 v128, v128
	v_lshlrev_b32_e32 v141, 16, v148
	v_lshlrev_b32_e32 v148, 16, v149
	v_mul_f32_e32 v121, v121, v150
	v_mul_f32_e32 v128, v128, v120
	v_mul_f32_e32 v120, v125, v146
	v_mul_f32_e32 v125, 0xbfb8aa3b, v147
	v_exp_f32_e32 v125, v125
	s_waitcnt vmcnt(0)
	v_mul_f32_e32 v120, v133, v120
	v_mul_f32_e32 v120, v120, v147
	v_lshlrev_b32_e32 v153, 16, v151
	v_add_f32_e32 v125, 1.0, v125
	v_rcp_f32_e32 v125, v125
	v_mul_f32_e32 v122, v130, v122
	v_and_b32_e32 v149, 0xffff0000, v149
	v_mul_f32_e32 v122, v122, v153
	v_mul_f32_e32 v120, v125, v120
	v_mul_f32_e32 v125, 0xbfb8aa3b, v150
	v_exp_f32_e32 v125, v125
	v_and_b32_e32 v151, 0xffff0000, v151
	v_mul_f32_e32 v124, v132, v124
	v_mul_f32_e32 v132, 0xbfb8aa3b, v141
	v_add_f32_e32 v125, 1.0, v125
	v_rcp_f32_e32 v125, v125
	v_exp_f32_e32 v132, v132
	v_mul_f32_e32 v123, v131, v123
	v_mul_f32_e32 v124, v124, v141
	v_mul_f32_e32 v125, v125, v121
	v_mul_f32_e32 v121, v126, v146
	v_mul_f32_e32 v126, 0xbfb8aa3b, v148
	v_exp_f32_e32 v126, v126
	v_mul_f32_e32 v121, v134, v121
	v_mul_f32_e32 v121, v121, v148
	v_add_f32_e32 v132, 1.0, v132
	v_add_f32_e32 v126, 1.0, v126
	v_rcp_f32_e32 v126, v126
	v_rcp_f32_e32 v132, v132
	v_mul_f32_e32 v123, v123, v151
	v_mul_f32_e32 v121, v126, v121
	v_mul_f32_e32 v126, 0xbfb8aa3b, v153
	v_exp_f32_e32 v126, v126
	v_mul_f32_e32 v124, v132, v124
	v_cvt_pk_bf16_f32 v120, v124, v120
	v_add_f32_e32 v126, 1.0, v126
	v_rcp_f32_e32 v126, v126
	s_nop 0
	v_mul_f32_e32 v126, v126, v122
	v_mul_f32_e32 v122, v127, v146
	v_mul_f32_e32 v127, 0xbfb8aa3b, v149
	v_exp_f32_e32 v127, v127
	v_mul_f32_e32 v122, v135, v122
	v_mul_f32_e32 v122, v122, v149
	v_add_f32_e32 v127, 1.0, v127
	v_rcp_f32_e32 v127, v127
	s_nop 0
	v_mul_f32_e32 v122, v127, v122
	v_mul_f32_e32 v127, 0xbfb8aa3b, v151
	v_exp_f32_e32 v127, v127
	v_cvt_pk_bf16_f32 v121, v121, v122
	v_cvt_pk_bf16_f32 v122, v128, v125
	v_lshl_add_u64 v[128:129], v[144:145], 0, v[138:139]
	v_add_f32_e32 v127, 1.0, v127
	v_rcp_f32_e32 v127, v127
	s_nop 0
	v_mul_f32_e32 v123, v127, v123
	v_cvt_pk_bf16_f32 v123, v126, v123
	global_store_dwordx4 v[128:129], v[120:123], off
	global_load_dwordx4 v[130:133], v[142:143], off offset:256 nt
	s_nop 0
	global_load_dwordx4 v[120:123], v[136:137], off offset:528
	global_load_dwordx4 v[124:127], v[136:137], off offset:512
	s_waitcnt vmcnt(2)
	v_lshlrev_b32_e32 v141, 16, v132
	s_waitcnt vmcnt(1)
	v_mul_f32_e32 v112, v112, v120
	v_mul_f32_e32 v120, 0xbfb8aa3b, v141
	v_exp_f32_e32 v120, v120
	v_lshlrev_b32_e32 v134, 16, v130
	v_and_b32_e32 v130, 0xffff0000, v130
	v_mul_f32_e32 v112, v112, v141
	v_add_f32_e32 v120, 1.0, v120
	v_rcp_f32_e32 v120, v120
	v_and_b32_e32 v132, 0xffff0000, v132
	v_mul_f32_e32 v113, v113, v121
	v_lshlrev_b32_e32 v135, 16, v131
	v_mul_f32_e32 v120, v112, v120
	v_mul_f32_e32 v112, v117, v146
	v_mul_f32_e32 v117, 0xbfb8aa3b, v130
	v_exp_f32_e32 v117, v117
	s_waitcnt vmcnt(0)
	v_mul_f32_e32 v112, v112, v125
	v_mul_f32_e32 v112, v112, v130
	v_mul_f32_e32 v113, v113, v132
	v_add_f32_e32 v117, 1.0, v117
	v_rcp_f32_e32 v117, v117
	v_lshlrev_b32_e32 v144, 16, v133
	v_mul_f32_e32 v114, v114, v122
	v_and_b32_e32 v131, 0xffff0000, v131
	v_mul_f32_e32 v112, v112, v117
	v_mul_f32_e32 v117, 0xbfb8aa3b, v132
	v_exp_f32_e32 v117, v117
	v_mul_f32_e32 v114, v114, v144
	v_and_b32_e32 v133, 0xffff0000, v133
	v_mul_f32_e32 v116, v116, v124
	v_add_f32_e32 v117, 1.0, v117
	v_rcp_f32_e32 v117, v117
	v_mul_f32_e32 v124, 0xbfb8aa3b, v134
	v_exp_f32_e32 v124, v124
	v_mul_f32_e32 v115, v115, v123
	v_mul_f32_e32 v117, v113, v117
	v_mul_f32_e32 v113, v118, v146
	v_mul_f32_e32 v118, 0xbfb8aa3b, v135
	v_exp_f32_e32 v118, v118
	v_mul_f32_e32 v113, v113, v126
	v_mul_f32_e32 v113, v113, v135
	v_add_f32_e32 v124, 1.0, v124
	v_add_f32_e32 v118, 1.0, v118
	v_rcp_f32_e32 v118, v118
	v_rcp_f32_e32 v124, v124
	v_mul_f32_e32 v115, v115, v133
	v_mul_f32_e32 v116, v116, v134
	v_mul_f32_e32 v113, v113, v118
	v_mul_f32_e32 v118, 0xbfb8aa3b, v144
	v_exp_f32_e32 v118, v118
	v_mul_f32_e32 v116, v116, v124
	v_cvt_pk_bf16_f32 v112, v116, v112
	v_add_f32_e32 v118, 1.0, v118
	v_rcp_f32_e32 v118, v118
	s_nop 0
	v_mul_f32_e32 v118, v114, v118
	v_mul_f32_e32 v114, v119, v146
	v_mul_f32_e32 v119, 0xbfb8aa3b, v131
	v_exp_f32_e32 v119, v119
	v_mul_f32_e32 v114, v114, v127
	v_mul_f32_e32 v114, v114, v131
	v_add_f32_e32 v119, 1.0, v119
	v_rcp_f32_e32 v119, v119
	s_nop 0
	v_mul_f32_e32 v114, v114, v119
	v_mul_f32_e32 v119, 0xbfb8aa3b, v133
	v_exp_f32_e32 v119, v119
	v_cvt_pk_bf16_f32 v113, v113, v114
	v_cvt_pk_bf16_f32 v114, v120, v117
	s_nop 0
	v_add_f32_e32 v119, 1.0, v119
	v_rcp_f32_e32 v119, v119
	s_nop 0
	v_mul_f32_e32 v115, v115, v119
	v_cvt_pk_bf16_f32 v115, v118, v115
	global_store_dwordx4 v[128:129], v[112:115], off offset:256
	global_load_dwordx4 v[120:123], v[142:143], off offset:512 nt
	s_nop 0
	global_load_dwordx4 v[112:115], v[136:137], off offset:1040
	global_load_dwordx4 v[116:119], v[136:137], off offset:1024
	s_waitcnt vmcnt(2)
	v_lshlrev_b32_e32 v126, 16, v122
	s_waitcnt vmcnt(1)
	v_mul_f32_e32 v104, v104, v112
	v_mul_f32_e32 v112, 0xbfb8aa3b, v126
	v_exp_f32_e32 v112, v112
	v_lshlrev_b32_e32 v124, 16, v120
	v_and_b32_e32 v120, 0xffff0000, v120
	v_mul_f32_e32 v104, v104, v126
	v_add_f32_e32 v112, 1.0, v112
	v_rcp_f32_e32 v112, v112
	v_and_b32_e32 v122, 0xffff0000, v122
	v_mul_f32_e32 v105, v105, v113
	v_lshlrev_b32_e32 v125, 16, v121
	v_mul_f32_e32 v112, v104, v112
	v_mul_f32_e32 v104, v109, v146
	v_mul_f32_e32 v109, 0xbfb8aa3b, v120
	v_exp_f32_e32 v109, v109
	s_waitcnt vmcnt(0)
	v_mul_f32_e32 v104, v104, v117
	v_mul_f32_e32 v104, v104, v120
	v_mul_f32_e32 v105, v105, v122
	v_add_f32_e32 v109, 1.0, v109
	v_rcp_f32_e32 v109, v109
	v_lshlrev_b32_e32 v127, 16, v123
	v_mul_f32_e32 v106, v106, v114
	v_and_b32_e32 v121, 0xffff0000, v121
	v_mul_f32_e32 v104, v104, v109
	v_mul_f32_e32 v109, 0xbfb8aa3b, v122
	v_exp_f32_e32 v109, v109
	v_mul_f32_e32 v106, v106, v127
	v_and_b32_e32 v123, 0xffff0000, v123
	v_mul_f32_e32 v108, v108, v116
	v_add_f32_e32 v109, 1.0, v109
	v_rcp_f32_e32 v109, v109
	v_mul_f32_e32 v116, 0xbfb8aa3b, v124
	v_exp_f32_e32 v116, v116
	v_mul_f32_e32 v107, v107, v115
	v_mul_f32_e32 v109, v105, v109
	v_mul_f32_e32 v105, v110, v146
	v_mul_f32_e32 v110, 0xbfb8aa3b, v125
	v_exp_f32_e32 v110, v110
	v_mul_f32_e32 v105, v105, v118
	v_mul_f32_e32 v105, v105, v125
	v_add_f32_e32 v116, 1.0, v116
	v_add_f32_e32 v110, 1.0, v110
	v_rcp_f32_e32 v110, v110
	v_rcp_f32_e32 v116, v116
	v_mul_f32_e32 v107, v107, v123
	v_mul_f32_e32 v108, v108, v124
	v_mul_f32_e32 v105, v105, v110
	v_mul_f32_e32 v110, 0xbfb8aa3b, v127
	v_exp_f32_e32 v110, v110
	v_mul_f32_e32 v108, v108, v116
	v_cvt_pk_bf16_f32 v104, v108, v104
	v_add_f32_e32 v110, 1.0, v110
	v_rcp_f32_e32 v110, v110
	s_nop 0
	v_mul_f32_e32 v110, v106, v110
	v_mul_f32_e32 v106, v111, v146
	v_mul_f32_e32 v111, 0xbfb8aa3b, v121
	v_exp_f32_e32 v111, v111
	v_mul_f32_e32 v106, v106, v119
	v_mul_f32_e32 v106, v106, v121
	v_add_f32_e32 v111, 1.0, v111
	v_rcp_f32_e32 v111, v111
	s_nop 0
	v_mul_f32_e32 v106, v106, v111
	v_mul_f32_e32 v111, 0xbfb8aa3b, v123
	v_exp_f32_e32 v111, v111
	v_cvt_pk_bf16_f32 v105, v105, v106
	v_cvt_pk_bf16_f32 v106, v112, v109
	s_nop 0
	v_add_f32_e32 v111, 1.0, v111
	v_rcp_f32_e32 v111, v111
	s_nop 0
	v_mul_f32_e32 v107, v107, v111
	v_cvt_pk_bf16_f32 v107, v110, v107
	global_store_dwordx4 v[128:129], v[104:107], off offset:512
	global_load_dwordx4 v[104:107], v[142:143], off offset:768 nt
	s_nop 0
	global_load_dwordx4 v[108:111], v[136:137], off offset:1552
	global_load_dwordx4 v[112:115], v[136:137], off offset:1536
	s_waitcnt vmcnt(2)
	v_lshlrev_b32_e32 v118, 16, v106
	s_waitcnt vmcnt(1)
	v_mul_f32_e32 v96, v96, v108
	v_mul_f32_e32 v108, 0xbfb8aa3b, v118
	v_exp_f32_e32 v108, v108
	v_lshlrev_b32_e32 v116, 16, v104
	v_and_b32_e32 v104, 0xffff0000, v104
	v_mul_f32_e32 v96, v96, v118
	v_add_f32_e32 v108, 1.0, v108
	v_rcp_f32_e32 v108, v108
	v_and_b32_e32 v106, 0xffff0000, v106
	v_mul_f32_e32 v97, v97, v109
	v_lshlrev_b32_e32 v117, 16, v105
	v_mul_f32_e32 v108, v96, v108
	v_mul_f32_e32 v96, v101, v146
	v_mul_f32_e32 v101, 0xbfb8aa3b, v104
	v_exp_f32_e32 v101, v101
	s_waitcnt vmcnt(0)
	v_mul_f32_e32 v96, v96, v113
	v_mul_f32_e32 v96, v96, v104
	v_mul_f32_e32 v97, v97, v106
	v_add_f32_e32 v101, 1.0, v101
	v_rcp_f32_e32 v101, v101
	v_lshlrev_b32_e32 v119, 16, v107
	v_mul_f32_e32 v98, v98, v110
	v_and_b32_e32 v105, 0xffff0000, v105
	v_mul_f32_e32 v96, v96, v101
	v_mul_f32_e32 v101, 0xbfb8aa3b, v106
	v_exp_f32_e32 v101, v101
	v_mul_f32_e32 v98, v98, v119
	v_and_b32_e32 v107, 0xffff0000, v107
	v_mul_f32_e32 v100, v100, v112
	v_add_f32_e32 v101, 1.0, v101
	v_rcp_f32_e32 v101, v101
	v_mul_f32_e32 v112, 0xbfb8aa3b, v116
	v_exp_f32_e32 v112, v112
	v_mul_f32_e32 v100, v100, v116
	v_mul_f32_e32 v101, v97, v101
	v_mul_f32_e32 v97, v102, v146
	v_mul_f32_e32 v102, 0xbfb8aa3b, v117
	v_exp_f32_e32 v102, v102
	v_mul_f32_e32 v97, v97, v114
	v_mul_f32_e32 v97, v97, v117
	v_add_f32_e32 v112, 1.0, v112
	v_add_f32_e32 v102, 1.0, v102
	v_rcp_f32_e32 v102, v102
	v_rcp_f32_e32 v112, v112
	v_mul_f32_e32 v99, v99, v111
	v_mul_f32_e32 v99, v99, v107
	v_mul_f32_e32 v97, v97, v102
	v_mul_f32_e32 v102, 0xbfb8aa3b, v119
	v_exp_f32_e32 v102, v102
	v_mul_f32_e32 v100, v100, v112
	v_cvt_pk_bf16_f32 v96, v100, v96
	v_or_b32_e32 v100, 16, v140
	v_add_f32_e32 v102, 1.0, v102
	v_rcp_f32_e32 v102, v102
	s_nop 0
	v_mul_f32_e32 v102, v98, v102
	v_mul_f32_e32 v98, v103, v146
	v_mul_f32_e32 v103, 0xbfb8aa3b, v105
	v_exp_f32_e32 v103, v103
	v_mul_f32_e32 v98, v98, v115
	v_mul_f32_e32 v98, v98, v105
	v_add_f32_e32 v103, 1.0, v103
	v_rcp_f32_e32 v103, v103
	s_nop 0
	v_mul_f32_e32 v98, v98, v103
	v_mul_f32_e32 v103, 0xbfb8aa3b, v107
	v_exp_f32_e32 v103, v103
	v_cvt_pk_bf16_f32 v97, v97, v98
	v_cvt_pk_bf16_f32 v98, v108, v101
	v_ashrrev_i32_e32 v101, 31, v100
	v_add_f32_e32 v103, 1.0, v103
	v_rcp_f32_e32 v103, v103
	s_nop 0
	v_mul_f32_e32 v99, v99, v103
	v_cvt_pk_bf16_f32 v99, v102, v99
	global_store_dwordx4 v[128:129], v[96:99], off offset:768
	s_nop 1
	v_lshl_add_u32 v96, v100, 4, s0
	ds_read_b128 v[96:99], v96
	s_waitcnt lgkmcnt(0)
	v_mov_b32_e32 v102, v97
	v_mov_b32_e32 v103, v98
	v_mov_b32_e32 v97, v99
	v_pk_add_f32 v[96:97], v[102:103], v[96:97]
	s_nop 0
	v_add_f32_e32 v96, v96, v97
	v_fmamk_f32 v96, v96, 0x3b000000, v189
	v_rsq_f32_e32 v108, v96
	v_lshl_add_u64 v[96:97], s[20:21], 0, v[100:101]
	v_lshlrev_b64 v[96:97], 13, v[96:97]
	v_lshl_add_u64 v[98:99], s[66:67], 0, v[96:97]
	v_lshl_add_u64 v[104:105], v[98:99], 0, v[138:139]
	v_lshl_add_u64 v[106:107], s[34:35], 0, v[96:97]
	global_load_dwordx4 v[110:113], v[104:105], off nt
	global_load_dwordx4 v[96:99], v[136:137], off offset:16
	global_load_dwordx4 v[100:103], v[136:137], off
	v_mul_f32_e32 v88, v88, v108
	v_mul_f32_e32 v89, v89, v108
	v_mul_f32_e32 v90, v90, v108
	v_mul_f32_e32 v92, v92, v108
	v_mul_f32_e32 v91, v91, v108
	v_mul_f32_e32 v80, v80, v108
	v_mul_f32_e32 v81, v81, v108
	v_mul_f32_e32 v82, v82, v108
	v_mul_f32_e32 v84, v84, v108
	v_mul_f32_e32 v83, v83, v108
	v_mul_f32_e32 v72, v72, v108
	v_mul_f32_e32 v73, v73, v108
	v_mul_f32_e32 v74, v74, v108
	v_mul_f32_e32 v76, v76, v108
	v_mul_f32_e32 v75, v75, v108
	v_mul_f32_e32 v64, v64, v108
	v_mul_f32_e32 v65, v65, v108
	v_mul_f32_e32 v66, v66, v108
	v_mul_f32_e32 v68, v68, v108
	v_mul_f32_e32 v67, v67, v108
	s_waitcnt vmcnt(2)
	v_lshlrev_b32_e32 v115, 16, v112
	s_waitcnt vmcnt(1)
	v_mul_f32_e32 v88, v96, v88
	v_mul_f32_e32 v96, 0xbfb8aa3b, v115
	v_exp_f32_e32 v96, v96
	v_lshlrev_b32_e32 v109, 16, v110
	v_and_b32_e32 v110, 0xffff0000, v110
	v_mul_f32_e32 v88, v88, v115
	v_add_f32_e32 v96, 1.0, v96
	v_rcp_f32_e32 v96, v96
	v_and_b32_e32 v112, 0xffff0000, v112
	v_mul_f32_e32 v89, v97, v89
	v_lshlrev_b32_e32 v114, 16, v111
	v_mul_f32_e32 v96, v96, v88
	v_mul_f32_e32 v88, v93, v108
	v_mul_f32_e32 v93, 0xbfb8aa3b, v110
	v_exp_f32_e32 v93, v93
	s_waitcnt vmcnt(0)
	v_mul_f32_e32 v88, v101, v88
	v_mul_f32_e32 v88, v88, v110
	v_mul_f32_e32 v89, v89, v112
	v_add_f32_e32 v93, 1.0, v93
	v_rcp_f32_e32 v93, v93
	v_lshlrev_b32_e32 v116, 16, v113
	v_mul_f32_e32 v90, v98, v90
	v_and_b32_e32 v111, 0xffff0000, v111
	v_mul_f32_e32 v88, v93, v88
	v_mul_f32_e32 v93, 0xbfb8aa3b, v112
	v_exp_f32_e32 v93, v93
	v_mul_f32_e32 v90, v90, v116
	v_and_b32_e32 v113, 0xffff0000, v113
	v_mul_f32_e32 v92, v100, v92
	v_add_f32_e32 v93, 1.0, v93
	v_rcp_f32_e32 v93, v93
	v_mul_f32_e32 v100, 0xbfb8aa3b, v109
	v_exp_f32_e32 v100, v100
	v_mul_f32_e32 v91, v99, v91
	v_mul_f32_e32 v93, v93, v89
	v_mul_f32_e32 v89, v94, v108
	v_mul_f32_e32 v94, 0xbfb8aa3b, v114
	v_exp_f32_e32 v94, v94
	v_mul_f32_e32 v89, v102, v89
	v_mul_f32_e32 v89, v89, v114
	v_add_f32_e32 v100, 1.0, v100
	v_add_f32_e32 v94, 1.0, v94
	v_rcp_f32_e32 v94, v94
	v_rcp_f32_e32 v100, v100
	v_mul_f32_e32 v92, v92, v109
	v_mul_f32_e32 v91, v91, v113
	v_mul_f32_e32 v89, v94, v89
	v_mul_f32_e32 v94, 0xbfb8aa3b, v116
	v_exp_f32_e32 v94, v94
	v_mul_f32_e32 v92, v100, v92
	v_cvt_pk_bf16_f32 v88, v92, v88
	v_add_f32_e32 v94, 1.0, v94
	v_rcp_f32_e32 v94, v94
	s_nop 0
	v_mul_f32_e32 v94, v94, v90
	v_mul_f32_e32 v90, v95, v108
	v_mul_f32_e32 v95, 0xbfb8aa3b, v111
	v_exp_f32_e32 v95, v95
	v_mul_f32_e32 v90, v103, v90
	v_mul_f32_e32 v90, v90, v111
	v_add_f32_e32 v95, 1.0, v95
	v_rcp_f32_e32 v95, v95
	s_nop 0
	v_mul_f32_e32 v90, v95, v90
	v_mul_f32_e32 v95, 0xbfb8aa3b, v113
	v_exp_f32_e32 v95, v95
	v_cvt_pk_bf16_f32 v89, v89, v90
	v_cvt_pk_bf16_f32 v90, v96, v93
	v_lshl_add_u64 v[96:97], v[106:107], 0, v[138:139]
	v_add_f32_e32 v95, 1.0, v95
	v_rcp_f32_e32 v95, v95
	s_nop 0
	v_mul_f32_e32 v91, v95, v91
	v_cvt_pk_bf16_f32 v91, v94, v91
	global_store_dwordx4 v[96:97], v[88:91], off
	global_load_dwordx4 v[98:101], v[104:105], off offset:256 nt
	s_nop 0
	global_load_dwordx4 v[88:91], v[136:137], off offset:528
	global_load_dwordx4 v[92:95], v[136:137], off offset:512
	s_waitcnt vmcnt(2)
	v_lshlrev_b32_e32 v106, 16, v100
	s_waitcnt vmcnt(1)
	v_mul_f32_e32 v80, v80, v88
	v_mul_f32_e32 v88, 0xbfb8aa3b, v106
	v_exp_f32_e32 v88, v88
	v_lshlrev_b32_e32 v102, 16, v98
	v_and_b32_e32 v98, 0xffff0000, v98
	v_mul_f32_e32 v80, v80, v106
	v_add_f32_e32 v88, 1.0, v88
	v_rcp_f32_e32 v88, v88
	v_and_b32_e32 v100, 0xffff0000, v100
	v_mul_f32_e32 v81, v81, v89
	v_lshlrev_b32_e32 v103, 16, v99
	v_mul_f32_e32 v88, v80, v88
	v_mul_f32_e32 v80, v85, v108
	v_mul_f32_e32 v85, 0xbfb8aa3b, v98
	v_exp_f32_e32 v85, v85
	s_waitcnt vmcnt(0)
	v_mul_f32_e32 v80, v80, v93
	v_mul_f32_e32 v80, v80, v98
	v_mul_f32_e32 v81, v81, v100
	v_add_f32_e32 v85, 1.0, v85
	v_rcp_f32_e32 v85, v85
	v_lshlrev_b32_e32 v107, 16, v101
	v_mul_f32_e32 v82, v82, v90
	v_and_b32_e32 v99, 0xffff0000, v99
	v_mul_f32_e32 v80, v80, v85
	v_mul_f32_e32 v85, 0xbfb8aa3b, v100
	v_exp_f32_e32 v85, v85
	v_mul_f32_e32 v82, v82, v107
	v_and_b32_e32 v101, 0xffff0000, v101
	v_mul_f32_e32 v84, v84, v92
	v_add_f32_e32 v85, 1.0, v85
	v_rcp_f32_e32 v85, v85
	v_mul_f32_e32 v92, 0xbfb8aa3b, v102
	v_exp_f32_e32 v92, v92
	v_mul_f32_e32 v83, v83, v91
	v_mul_f32_e32 v85, v81, v85
	v_mul_f32_e32 v81, v86, v108
	v_mul_f32_e32 v86, 0xbfb8aa3b, v103
	v_exp_f32_e32 v86, v86
	v_mul_f32_e32 v81, v81, v94
	v_mul_f32_e32 v81, v81, v103
	v_add_f32_e32 v92, 1.0, v92
	v_add_f32_e32 v86, 1.0, v86
	v_rcp_f32_e32 v86, v86
	v_rcp_f32_e32 v92, v92
	v_mul_f32_e32 v83, v83, v101
	v_mul_f32_e32 v84, v84, v102
	v_mul_f32_e32 v81, v81, v86
	v_mul_f32_e32 v86, 0xbfb8aa3b, v107
	v_exp_f32_e32 v86, v86
	v_mul_f32_e32 v84, v84, v92
	v_cvt_pk_bf16_f32 v80, v84, v80
	v_add_f32_e32 v86, 1.0, v86
	v_rcp_f32_e32 v86, v86
	s_nop 0
	v_mul_f32_e32 v86, v82, v86
	v_mul_f32_e32 v82, v87, v108
	v_mul_f32_e32 v87, 0xbfb8aa3b, v99
	v_exp_f32_e32 v87, v87
	v_mul_f32_e32 v82, v82, v95
	v_mul_f32_e32 v82, v82, v99
	v_add_f32_e32 v87, 1.0, v87
	v_rcp_f32_e32 v87, v87
	s_nop 0
	v_mul_f32_e32 v82, v82, v87
	v_mul_f32_e32 v87, 0xbfb8aa3b, v101
	v_exp_f32_e32 v87, v87
	v_cvt_pk_bf16_f32 v81, v81, v82
	v_cvt_pk_bf16_f32 v82, v88, v85
	s_nop 0
	v_add_f32_e32 v87, 1.0, v87
	v_rcp_f32_e32 v87, v87
	s_nop 0
	v_mul_f32_e32 v83, v83, v87
	v_cvt_pk_bf16_f32 v83, v86, v83
	global_store_dwordx4 v[96:97], v[80:83], off offset:256
	global_load_dwordx4 v[88:91], v[104:105], off offset:512 nt
	s_nop 0
	global_load_dwordx4 v[80:83], v[136:137], off offset:1040
	global_load_dwordx4 v[84:87], v[136:137], off offset:1024
	s_waitcnt vmcnt(2)
	v_lshlrev_b32_e32 v94, 16, v90
	s_waitcnt vmcnt(1)
	v_mul_f32_e32 v72, v72, v80
	v_mul_f32_e32 v80, 0xbfb8aa3b, v94
	v_exp_f32_e32 v80, v80
	v_lshlrev_b32_e32 v92, 16, v88
	v_and_b32_e32 v88, 0xffff0000, v88
	v_mul_f32_e32 v72, v72, v94
	v_add_f32_e32 v80, 1.0, v80
	v_rcp_f32_e32 v80, v80
	v_and_b32_e32 v90, 0xffff0000, v90
	v_mul_f32_e32 v73, v73, v81
	v_lshlrev_b32_e32 v93, 16, v89
	v_mul_f32_e32 v80, v72, v80
	v_mul_f32_e32 v72, v77, v108
	v_mul_f32_e32 v77, 0xbfb8aa3b, v88
	v_exp_f32_e32 v77, v77
	s_waitcnt vmcnt(0)
	v_mul_f32_e32 v72, v72, v85
	v_mul_f32_e32 v72, v72, v88
	v_mul_f32_e32 v73, v73, v90
	v_add_f32_e32 v77, 1.0, v77
	v_rcp_f32_e32 v77, v77
	v_lshlrev_b32_e32 v95, 16, v91
	v_mul_f32_e32 v74, v74, v82
	v_and_b32_e32 v89, 0xffff0000, v89
	v_mul_f32_e32 v72, v72, v77
	v_mul_f32_e32 v77, 0xbfb8aa3b, v90
	v_exp_f32_e32 v77, v77
	v_mul_f32_e32 v74, v74, v95
	v_and_b32_e32 v91, 0xffff0000, v91
	v_mul_f32_e32 v76, v76, v84
	v_add_f32_e32 v77, 1.0, v77
	v_rcp_f32_e32 v77, v77
	v_mul_f32_e32 v84, 0xbfb8aa3b, v92
	v_exp_f32_e32 v84, v84
	v_mul_f32_e32 v75, v75, v83
	v_mul_f32_e32 v77, v73, v77
	v_mul_f32_e32 v73, v78, v108
	v_mul_f32_e32 v78, 0xbfb8aa3b, v93
	v_exp_f32_e32 v78, v78
	v_mul_f32_e32 v73, v73, v86
	v_mul_f32_e32 v73, v73, v93
	v_add_f32_e32 v84, 1.0, v84
	v_add_f32_e32 v78, 1.0, v78
	v_rcp_f32_e32 v78, v78
	v_rcp_f32_e32 v84, v84
	v_mul_f32_e32 v75, v75, v91
	v_mul_f32_e32 v76, v76, v92
	v_mul_f32_e32 v73, v73, v78
	v_mul_f32_e32 v78, 0xbfb8aa3b, v95
	v_exp_f32_e32 v78, v78
	v_mul_f32_e32 v76, v76, v84
	v_cvt_pk_bf16_f32 v72, v76, v72
	v_add_f32_e32 v78, 1.0, v78
	v_rcp_f32_e32 v78, v78
	s_nop 0
	v_mul_f32_e32 v78, v74, v78
	v_mul_f32_e32 v74, v79, v108
	v_mul_f32_e32 v79, 0xbfb8aa3b, v89
	v_exp_f32_e32 v79, v79
	v_mul_f32_e32 v74, v74, v87
	v_mul_f32_e32 v74, v74, v89
	v_add_f32_e32 v79, 1.0, v79
	v_rcp_f32_e32 v79, v79
	s_nop 0
	v_mul_f32_e32 v74, v74, v79
	v_mul_f32_e32 v79, 0xbfb8aa3b, v91
	v_exp_f32_e32 v79, v79
	v_cvt_pk_bf16_f32 v73, v73, v74
	v_cvt_pk_bf16_f32 v74, v80, v77
	s_nop 0
	v_add_f32_e32 v79, 1.0, v79
	v_rcp_f32_e32 v79, v79
	s_nop 0
	v_mul_f32_e32 v75, v75, v79
	v_cvt_pk_bf16_f32 v75, v78, v75
	global_store_dwordx4 v[96:97], v[72:75], off offset:512
	global_load_dwordx4 v[72:75], v[104:105], off offset:768 nt
	s_nop 0
	global_load_dwordx4 v[76:79], v[136:137], off offset:1552
	global_load_dwordx4 v[80:83], v[136:137], off offset:1536
	s_waitcnt vmcnt(2)
	v_lshlrev_b32_e32 v86, 16, v74
	s_waitcnt vmcnt(1)
	v_mul_f32_e32 v64, v64, v76
	v_mul_f32_e32 v76, 0xbfb8aa3b, v86
	v_exp_f32_e32 v76, v76
	v_lshlrev_b32_e32 v84, 16, v72
	v_and_b32_e32 v72, 0xffff0000, v72
	v_mul_f32_e32 v64, v64, v86
	v_add_f32_e32 v76, 1.0, v76
	v_rcp_f32_e32 v76, v76
	v_and_b32_e32 v74, 0xffff0000, v74
	v_mul_f32_e32 v65, v65, v77
	v_lshlrev_b32_e32 v85, 16, v73
	v_mul_f32_e32 v76, v64, v76
	v_mul_f32_e32 v64, v69, v108
	v_mul_f32_e32 v69, 0xbfb8aa3b, v72
	v_exp_f32_e32 v69, v69
	s_waitcnt vmcnt(0)
	v_mul_f32_e32 v64, v64, v81
	v_mul_f32_e32 v64, v64, v72
	v_mul_f32_e32 v65, v65, v74
	v_add_f32_e32 v69, 1.0, v69
	v_rcp_f32_e32 v69, v69
	v_lshlrev_b32_e32 v87, 16, v75
	v_mul_f32_e32 v66, v66, v78
	v_and_b32_e32 v73, 0xffff0000, v73
	v_mul_f32_e32 v64, v64, v69
	v_mul_f32_e32 v69, 0xbfb8aa3b, v74
	v_exp_f32_e32 v69, v69
	v_mul_f32_e32 v66, v66, v87
	v_and_b32_e32 v75, 0xffff0000, v75
	v_mul_f32_e32 v68, v68, v80
	v_add_f32_e32 v69, 1.0, v69
	v_rcp_f32_e32 v69, v69
	v_mul_f32_e32 v80, 0xbfb8aa3b, v84
	v_exp_f32_e32 v80, v80
	v_mul_f32_e32 v68, v68, v84
	v_mul_f32_e32 v69, v65, v69
	v_mul_f32_e32 v65, v70, v108
	v_mul_f32_e32 v70, 0xbfb8aa3b, v85
	v_exp_f32_e32 v70, v70
	v_mul_f32_e32 v65, v65, v82
	v_mul_f32_e32 v65, v65, v85
	v_add_f32_e32 v80, 1.0, v80
	v_add_f32_e32 v70, 1.0, v70
	v_rcp_f32_e32 v70, v70
	v_rcp_f32_e32 v80, v80
	v_mul_f32_e32 v67, v67, v79
	v_mul_f32_e32 v67, v67, v75
	v_mul_f32_e32 v65, v65, v70
	v_mul_f32_e32 v70, 0xbfb8aa3b, v87
	v_exp_f32_e32 v70, v70
	v_mul_f32_e32 v68, v68, v80
	v_cvt_pk_bf16_f32 v64, v68, v64
	v_or_b32_e32 v68, 32, v140
	v_add_f32_e32 v70, 1.0, v70
	v_rcp_f32_e32 v70, v70
	s_nop 0
	v_mul_f32_e32 v70, v66, v70
	v_mul_f32_e32 v66, v71, v108
	v_mul_f32_e32 v71, 0xbfb8aa3b, v73
	v_exp_f32_e32 v71, v71
	v_mul_f32_e32 v66, v66, v83
	v_mul_f32_e32 v66, v66, v73
	v_add_f32_e32 v71, 1.0, v71
	v_rcp_f32_e32 v71, v71
	s_nop 0
	v_mul_f32_e32 v66, v66, v71
	v_mul_f32_e32 v71, 0xbfb8aa3b, v75
	v_exp_f32_e32 v71, v71
	v_cvt_pk_bf16_f32 v65, v65, v66
	v_cvt_pk_bf16_f32 v66, v76, v69
	v_ashrrev_i32_e32 v69, 31, v68
	v_add_f32_e32 v71, 1.0, v71
	v_rcp_f32_e32 v71, v71
	s_nop 0
	v_mul_f32_e32 v67, v67, v71
	v_cvt_pk_bf16_f32 v67, v70, v67
	global_store_dwordx4 v[96:97], v[64:67], off offset:768
	s_nop 1
	v_lshl_add_u32 v64, v68, 4, s0
	ds_read_b128 v[64:67], v64
	s_waitcnt lgkmcnt(0)
	v_mov_b32_e32 v70, v65
	v_mov_b32_e32 v71, v66
	v_mov_b32_e32 v65, v67
	v_pk_add_f32 v[64:65], v[70:71], v[64:65]
	s_nop 0
	v_add_f32_e32 v64, v64, v65
	v_fmamk_f32 v64, v64, 0x3b000000, v189
	v_rsq_f32_e32 v76, v64
	v_lshl_add_u64 v[64:65], s[20:21], 0, v[68:69]
	v_lshlrev_b64 v[64:65], 13, v[64:65]
	v_lshl_add_u64 v[66:67], s[66:67], 0, v[64:65]
	v_lshl_add_u64 v[72:73], v[66:67], 0, v[138:139]
	v_lshl_add_u64 v[74:75], s[34:35], 0, v[64:65]
	global_load_dwordx4 v[78:81], v[72:73], off nt
	global_load_dwordx4 v[64:67], v[136:137], off offset:16
	global_load_dwordx4 v[68:71], v[136:137], off
	v_mul_f32_e32 v56, v56, v76
	v_mul_f32_e32 v57, v57, v76
	v_mul_f32_e32 v58, v58, v76
	v_mul_f32_e32 v60, v60, v76
	v_mul_f32_e32 v59, v59, v76
	v_mul_f32_e32 v48, v48, v76
	v_mul_f32_e32 v49, v49, v76
	v_mul_f32_e32 v50, v50, v76
	v_mul_f32_e32 v52, v52, v76
	v_mul_f32_e32 v51, v51, v76
	v_mul_f32_e32 v40, v40, v76
	v_mul_f32_e32 v41, v41, v76
	v_mul_f32_e32 v42, v42, v76
	v_mul_f32_e32 v44, v44, v76
	v_mul_f32_e32 v43, v43, v76
	v_mul_f32_e32 v32, v32, v76
	v_mul_f32_e32 v33, v33, v76
	v_mul_f32_e32 v34, v34, v76
	v_mul_f32_e32 v36, v36, v76
	v_mul_f32_e32 v35, v35, v76
	s_waitcnt vmcnt(2)
	v_lshlrev_b32_e32 v83, 16, v80
	s_waitcnt vmcnt(1)
	v_mul_f32_e32 v56, v64, v56
	v_mul_f32_e32 v64, 0xbfb8aa3b, v83
	v_exp_f32_e32 v64, v64
	v_lshlrev_b32_e32 v77, 16, v78
	v_and_b32_e32 v78, 0xffff0000, v78
	v_mul_f32_e32 v56, v56, v83
	v_add_f32_e32 v64, 1.0, v64
	v_rcp_f32_e32 v64, v64
	v_and_b32_e32 v80, 0xffff0000, v80
	v_mul_f32_e32 v57, v65, v57
	v_lshlrev_b32_e32 v82, 16, v79
	v_mul_f32_e32 v64, v64, v56
	v_mul_f32_e32 v56, v61, v76
	v_mul_f32_e32 v61, 0xbfb8aa3b, v78
	v_exp_f32_e32 v61, v61
	s_waitcnt vmcnt(0)
	v_mul_f32_e32 v56, v69, v56
	v_mul_f32_e32 v56, v56, v78
	v_mul_f32_e32 v57, v57, v80
	v_add_f32_e32 v61, 1.0, v61
	v_rcp_f32_e32 v61, v61
	v_lshlrev_b32_e32 v84, 16, v81
	v_mul_f32_e32 v58, v66, v58
	v_and_b32_e32 v79, 0xffff0000, v79
	v_mul_f32_e32 v56, v61, v56
	v_mul_f32_e32 v61, 0xbfb8aa3b, v80
	v_exp_f32_e32 v61, v61
	v_mul_f32_e32 v58, v58, v84
	v_and_b32_e32 v81, 0xffff0000, v81
	v_mul_f32_e32 v60, v68, v60
	v_add_f32_e32 v61, 1.0, v61
	v_rcp_f32_e32 v61, v61
	v_mul_f32_e32 v68, 0xbfb8aa3b, v77
	v_exp_f32_e32 v68, v68
	v_mul_f32_e32 v59, v67, v59
	v_mul_f32_e32 v61, v61, v57
	v_mul_f32_e32 v57, v62, v76
	v_mul_f32_e32 v62, 0xbfb8aa3b, v82
	v_exp_f32_e32 v62, v62
	v_mul_f32_e32 v57, v70, v57
	v_mul_f32_e32 v57, v57, v82
	v_add_f32_e32 v68, 1.0, v68
	v_add_f32_e32 v62, 1.0, v62
	v_rcp_f32_e32 v62, v62
	v_rcp_f32_e32 v68, v68
	v_mul_f32_e32 v60, v60, v77
	v_mul_f32_e32 v59, v59, v81
	v_mul_f32_e32 v57, v62, v57
	v_mul_f32_e32 v62, 0xbfb8aa3b, v84
	v_exp_f32_e32 v62, v62
	v_mul_f32_e32 v60, v68, v60
	v_cvt_pk_bf16_f32 v56, v60, v56
	v_add_f32_e32 v62, 1.0, v62
	v_rcp_f32_e32 v62, v62
	s_nop 0
	v_mul_f32_e32 v62, v62, v58
	v_mul_f32_e32 v58, v63, v76
	v_mul_f32_e32 v63, 0xbfb8aa3b, v79
	v_exp_f32_e32 v63, v63
	v_mul_f32_e32 v58, v71, v58
	v_mul_f32_e32 v58, v58, v79
	v_add_f32_e32 v63, 1.0, v63
	v_rcp_f32_e32 v63, v63
	s_nop 0
	v_mul_f32_e32 v58, v63, v58
	v_mul_f32_e32 v63, 0xbfb8aa3b, v81
	v_exp_f32_e32 v63, v63
	v_cvt_pk_bf16_f32 v57, v57, v58
	v_cvt_pk_bf16_f32 v58, v64, v61
	v_lshl_add_u64 v[64:65], v[74:75], 0, v[138:139]
	v_add_f32_e32 v63, 1.0, v63
	v_rcp_f32_e32 v63, v63
	s_nop 0
	v_mul_f32_e32 v59, v63, v59
	v_cvt_pk_bf16_f32 v59, v62, v59
	global_store_dwordx4 v[64:65], v[56:59], off
	global_load_dwordx4 v[66:69], v[72:73], off offset:256 nt
	s_nop 0
	global_load_dwordx4 v[56:59], v[136:137], off offset:528
	global_load_dwordx4 v[60:63], v[136:137], off offset:512
	s_waitcnt vmcnt(2)
	v_lshlrev_b32_e32 v74, 16, v68
	s_waitcnt vmcnt(1)
	v_mul_f32_e32 v48, v48, v56
	v_mul_f32_e32 v56, 0xbfb8aa3b, v74
	v_exp_f32_e32 v56, v56
	v_lshlrev_b32_e32 v70, 16, v66
	v_and_b32_e32 v66, 0xffff0000, v66
	v_mul_f32_e32 v48, v48, v74
	v_add_f32_e32 v56, 1.0, v56
	v_rcp_f32_e32 v56, v56
	v_and_b32_e32 v68, 0xffff0000, v68
	v_mul_f32_e32 v49, v49, v57
	v_lshlrev_b32_e32 v71, 16, v67
	v_mul_f32_e32 v56, v48, v56
	v_mul_f32_e32 v48, v53, v76
	v_mul_f32_e32 v53, 0xbfb8aa3b, v66
	v_exp_f32_e32 v53, v53
	s_waitcnt vmcnt(0)
	v_mul_f32_e32 v48, v48, v61
	v_mul_f32_e32 v48, v48, v66
	v_mul_f32_e32 v49, v49, v68
	v_add_f32_e32 v53, 1.0, v53
	v_rcp_f32_e32 v53, v53
	v_lshlrev_b32_e32 v75, 16, v69
	v_mul_f32_e32 v50, v50, v58
	v_and_b32_e32 v67, 0xffff0000, v67
	v_mul_f32_e32 v48, v48, v53
	v_mul_f32_e32 v53, 0xbfb8aa3b, v68
	v_exp_f32_e32 v53, v53
	v_mul_f32_e32 v50, v50, v75
	v_and_b32_e32 v69, 0xffff0000, v69
	v_mul_f32_e32 v52, v52, v60
	v_add_f32_e32 v53, 1.0, v53
	v_rcp_f32_e32 v53, v53
	v_mul_f32_e32 v60, 0xbfb8aa3b, v70
	v_exp_f32_e32 v60, v60
	v_mul_f32_e32 v51, v51, v59
	v_mul_f32_e32 v53, v49, v53
	v_mul_f32_e32 v49, v54, v76
	v_mul_f32_e32 v54, 0xbfb8aa3b, v71
	v_exp_f32_e32 v54, v54
	v_mul_f32_e32 v49, v49, v62
	v_mul_f32_e32 v49, v49, v71
	v_add_f32_e32 v60, 1.0, v60
	v_add_f32_e32 v54, 1.0, v54
	v_rcp_f32_e32 v54, v54
	v_rcp_f32_e32 v60, v60
	v_mul_f32_e32 v51, v51, v69
	v_mul_f32_e32 v52, v52, v70
	v_mul_f32_e32 v49, v49, v54
	v_mul_f32_e32 v54, 0xbfb8aa3b, v75
	v_exp_f32_e32 v54, v54
	v_mul_f32_e32 v52, v52, v60
	v_cvt_pk_bf16_f32 v48, v52, v48
	v_add_f32_e32 v54, 1.0, v54
	v_rcp_f32_e32 v54, v54
	s_nop 0
	v_mul_f32_e32 v54, v50, v54
	v_mul_f32_e32 v50, v55, v76
	v_mul_f32_e32 v55, 0xbfb8aa3b, v67
	v_exp_f32_e32 v55, v55
	v_mul_f32_e32 v50, v50, v63
	v_mul_f32_e32 v50, v50, v67
	v_add_f32_e32 v55, 1.0, v55
	v_rcp_f32_e32 v55, v55
	s_nop 0
	v_mul_f32_e32 v50, v50, v55
	v_mul_f32_e32 v55, 0xbfb8aa3b, v69
	v_exp_f32_e32 v55, v55
	v_cvt_pk_bf16_f32 v49, v49, v50
	v_cvt_pk_bf16_f32 v50, v56, v53
	s_nop 0
	v_add_f32_e32 v55, 1.0, v55
	v_rcp_f32_e32 v55, v55
	s_nop 0
	v_mul_f32_e32 v51, v51, v55
	v_cvt_pk_bf16_f32 v51, v54, v51
	global_store_dwordx4 v[64:65], v[48:51], off offset:256
	global_load_dwordx4 v[56:59], v[72:73], off offset:512 nt
	s_nop 0
	global_load_dwordx4 v[48:51], v[136:137], off offset:1040
	global_load_dwordx4 v[52:55], v[136:137], off offset:1024
	s_waitcnt vmcnt(2)
	v_lshlrev_b32_e32 v62, 16, v58
	s_waitcnt vmcnt(1)
	v_mul_f32_e32 v40, v40, v48
	v_mul_f32_e32 v48, 0xbfb8aa3b, v62
	v_exp_f32_e32 v48, v48
	v_lshlrev_b32_e32 v60, 16, v56
	v_and_b32_e32 v56, 0xffff0000, v56
	v_mul_f32_e32 v40, v40, v62
	v_add_f32_e32 v48, 1.0, v48
	v_rcp_f32_e32 v48, v48
	v_and_b32_e32 v58, 0xffff0000, v58
	v_mul_f32_e32 v41, v41, v49
	v_lshlrev_b32_e32 v61, 16, v57
	v_mul_f32_e32 v48, v40, v48
	v_mul_f32_e32 v40, v45, v76
	v_mul_f32_e32 v45, 0xbfb8aa3b, v56
	v_exp_f32_e32 v45, v45
	s_waitcnt vmcnt(0)
	v_mul_f32_e32 v40, v40, v53
	v_mul_f32_e32 v40, v40, v56
	v_mul_f32_e32 v41, v41, v58
	v_add_f32_e32 v45, 1.0, v45
	v_rcp_f32_e32 v45, v45
	v_lshlrev_b32_e32 v63, 16, v59
	v_mul_f32_e32 v42, v42, v50
	v_and_b32_e32 v57, 0xffff0000, v57
	v_mul_f32_e32 v40, v40, v45
	v_mul_f32_e32 v45, 0xbfb8aa3b, v58
	v_exp_f32_e32 v45, v45
	v_mul_f32_e32 v42, v42, v63
	v_and_b32_e32 v59, 0xffff0000, v59
	v_mul_f32_e32 v44, v44, v52
	v_add_f32_e32 v45, 1.0, v45
	v_rcp_f32_e32 v45, v45
	v_mul_f32_e32 v52, 0xbfb8aa3b, v60
	v_exp_f32_e32 v52, v52
	v_mul_f32_e32 v43, v43, v51
	v_mul_f32_e32 v45, v41, v45
	v_mul_f32_e32 v41, v46, v76
	v_mul_f32_e32 v46, 0xbfb8aa3b, v61
	v_exp_f32_e32 v46, v46
	v_mul_f32_e32 v41, v41, v54
	v_mul_f32_e32 v41, v41, v61
	v_add_f32_e32 v52, 1.0, v52
	v_add_f32_e32 v46, 1.0, v46
	v_rcp_f32_e32 v46, v46
	v_rcp_f32_e32 v52, v52
	v_mul_f32_e32 v43, v43, v59
	v_mul_f32_e32 v44, v44, v60
	v_mul_f32_e32 v41, v41, v46
	v_mul_f32_e32 v46, 0xbfb8aa3b, v63
	v_exp_f32_e32 v46, v46
	v_mul_f32_e32 v44, v44, v52
	v_cvt_pk_bf16_f32 v40, v44, v40
	v_add_f32_e32 v46, 1.0, v46
	v_rcp_f32_e32 v46, v46
	s_nop 0
	v_mul_f32_e32 v46, v42, v46
	v_mul_f32_e32 v42, v47, v76
	v_mul_f32_e32 v47, 0xbfb8aa3b, v57
	v_exp_f32_e32 v47, v47
	v_mul_f32_e32 v42, v42, v55
	v_mul_f32_e32 v42, v42, v57
	v_add_f32_e32 v47, 1.0, v47
	v_rcp_f32_e32 v47, v47
	s_nop 0
	v_mul_f32_e32 v42, v42, v47
	v_mul_f32_e32 v47, 0xbfb8aa3b, v59
	v_exp_f32_e32 v47, v47
	v_cvt_pk_bf16_f32 v41, v41, v42
	v_cvt_pk_bf16_f32 v42, v48, v45
	s_nop 0
	v_add_f32_e32 v47, 1.0, v47
	v_rcp_f32_e32 v47, v47
	s_nop 0
	v_mul_f32_e32 v43, v43, v47
	v_cvt_pk_bf16_f32 v43, v46, v43
	global_store_dwordx4 v[64:65], v[40:43], off offset:512
	global_load_dwordx4 v[40:43], v[72:73], off offset:768 nt
	s_nop 0
	global_load_dwordx4 v[44:47], v[136:137], off offset:1552
	global_load_dwordx4 v[48:51], v[136:137], off offset:1536
	s_waitcnt vmcnt(2)
	v_lshlrev_b32_e32 v54, 16, v42
	s_waitcnt vmcnt(1)
	v_mul_f32_e32 v32, v32, v44
	v_mul_f32_e32 v44, 0xbfb8aa3b, v54
	v_exp_f32_e32 v44, v44
	v_lshlrev_b32_e32 v52, 16, v40
	v_and_b32_e32 v40, 0xffff0000, v40
	v_mul_f32_e32 v32, v32, v54
	v_add_f32_e32 v44, 1.0, v44
	v_rcp_f32_e32 v44, v44
	v_and_b32_e32 v42, 0xffff0000, v42
	v_mul_f32_e32 v33, v33, v45
	v_lshlrev_b32_e32 v53, 16, v41
	v_mul_f32_e32 v44, v32, v44
	v_mul_f32_e32 v32, v37, v76
	v_mul_f32_e32 v37, 0xbfb8aa3b, v40
	v_exp_f32_e32 v37, v37
	s_waitcnt vmcnt(0)
	v_mul_f32_e32 v32, v32, v49
	v_mul_f32_e32 v32, v32, v40
	v_mul_f32_e32 v33, v33, v42
	v_add_f32_e32 v37, 1.0, v37
	v_rcp_f32_e32 v37, v37
	v_lshlrev_b32_e32 v55, 16, v43
	v_mul_f32_e32 v34, v34, v46
	v_and_b32_e32 v41, 0xffff0000, v41
	v_mul_f32_e32 v32, v32, v37
	v_mul_f32_e32 v37, 0xbfb8aa3b, v42
	v_exp_f32_e32 v37, v37
	v_mul_f32_e32 v34, v34, v55
	v_and_b32_e32 v43, 0xffff0000, v43
	v_mul_f32_e32 v36, v36, v48
	v_add_f32_e32 v37, 1.0, v37
	v_rcp_f32_e32 v37, v37
	v_mul_f32_e32 v48, 0xbfb8aa3b, v52
	v_exp_f32_e32 v48, v48
	v_mul_f32_e32 v36, v36, v52
	v_mul_f32_e32 v37, v33, v37
	v_mul_f32_e32 v33, v38, v76
	v_mul_f32_e32 v38, 0xbfb8aa3b, v53
	v_exp_f32_e32 v38, v38
	v_mul_f32_e32 v33, v33, v50
	v_mul_f32_e32 v33, v33, v53
	v_add_f32_e32 v48, 1.0, v48
	v_add_f32_e32 v38, 1.0, v38
	v_rcp_f32_e32 v38, v38
	v_rcp_f32_e32 v48, v48
	v_mul_f32_e32 v35, v35, v47
	v_mul_f32_e32 v35, v35, v43
	v_mul_f32_e32 v33, v33, v38
	v_mul_f32_e32 v38, 0xbfb8aa3b, v55
	v_exp_f32_e32 v38, v38
	v_mul_f32_e32 v36, v36, v48
	v_cvt_pk_bf16_f32 v32, v36, v32
	v_or_b32_e32 v36, 48, v140
	v_add_f32_e32 v38, 1.0, v38
	v_rcp_f32_e32 v38, v38
	s_nop 0
	v_mul_f32_e32 v38, v34, v38
	v_mul_f32_e32 v34, v39, v76
	v_mul_f32_e32 v39, 0xbfb8aa3b, v41
	v_exp_f32_e32 v39, v39
	v_mul_f32_e32 v34, v34, v51
	v_mul_f32_e32 v34, v34, v41
	v_add_f32_e32 v39, 1.0, v39
	v_rcp_f32_e32 v39, v39
	s_nop 0
	v_mul_f32_e32 v34, v34, v39
	v_mul_f32_e32 v39, 0xbfb8aa3b, v43
	v_exp_f32_e32 v39, v39
	v_cvt_pk_bf16_f32 v33, v33, v34
	v_cvt_pk_bf16_f32 v34, v44, v37
	v_ashrrev_i32_e32 v37, 31, v36
	v_add_f32_e32 v39, 1.0, v39
	v_rcp_f32_e32 v39, v39
	s_nop 0
	v_mul_f32_e32 v35, v35, v39
	v_cvt_pk_bf16_f32 v35, v38, v35
	global_store_dwordx4 v[64:65], v[32:35], off offset:768
	s_nop 1
	v_lshl_add_u32 v32, v36, 4, s0
	ds_read_b128 v[32:35], v32
	s_mov_b64 s[0:1], 0
	s_waitcnt lgkmcnt(0)
	v_mov_b32_e32 v38, v33
	v_mov_b32_e32 v39, v34
	v_mov_b32_e32 v33, v35
	v_pk_add_f32 v[32:33], v[38:39], v[32:33]
	s_nop 0
	v_add_f32_e32 v32, v32, v33
	v_fmamk_f32 v32, v32, 0x3b000000, v189
	v_rsq_f32_e32 v44, v32
	v_lshl_add_u64 v[32:33], s[20:21], 0, v[36:37]
	v_lshlrev_b64 v[32:33], 13, v[32:33]
	v_lshl_add_u64 v[34:35], s[66:67], 0, v[32:33]
	v_lshl_add_u64 v[40:41], v[34:35], 0, v[138:139]
	v_lshl_add_u64 v[42:43], s[34:35], 0, v[32:33]
	global_load_dwordx4 v[46:49], v[40:41], off nt
	global_load_dwordx4 v[32:35], v[136:137], off offset:16
	global_load_dwordx4 v[36:39], v[136:137], off
	v_mul_f32_e32 v24, v24, v44
	v_mul_f32_e32 v25, v25, v44
	v_mul_f32_e32 v26, v26, v44
	v_mul_f32_e32 v28, v28, v44
	v_mul_f32_e32 v27, v27, v44
	v_mul_f32_e32 v16, v16, v44
	v_mul_f32_e32 v17, v17, v44
	v_mul_f32_e32 v18, v18, v44
	v_mul_f32_e32 v20, v20, v44
	v_mul_f32_e32 v19, v19, v44
	v_mul_f32_e32 v8, v8, v44
	v_mul_f32_e32 v9, v9, v44
	v_mul_f32_e32 v10, v10, v44
	v_mul_f32_e32 v12, v12, v44
	v_mul_f32_e32 v11, v11, v44
	v_mul_f32_e32 v0, v0, v44
	v_mul_f32_e32 v1, v1, v44
	v_mul_f32_e32 v2, v2, v44
	v_mul_f32_e32 v4, v4, v44
	v_mul_f32_e32 v3, v3, v44
	s_waitcnt vmcnt(2)
	v_lshlrev_b32_e32 v51, 16, v48
	s_waitcnt vmcnt(1)
	v_mul_f32_e32 v24, v32, v24
	v_mul_f32_e32 v32, 0xbfb8aa3b, v51
	v_exp_f32_e32 v32, v32
	v_lshlrev_b32_e32 v45, 16, v46
	v_and_b32_e32 v46, 0xffff0000, v46
	v_mul_f32_e32 v24, v24, v51
	v_add_f32_e32 v32, 1.0, v32
	v_rcp_f32_e32 v32, v32
	v_and_b32_e32 v48, 0xffff0000, v48
	v_mul_f32_e32 v25, v33, v25
	v_lshlrev_b32_e32 v50, 16, v47
	v_mul_f32_e32 v32, v32, v24
	v_mul_f32_e32 v24, v29, v44
	v_mul_f32_e32 v29, 0xbfb8aa3b, v46
	v_exp_f32_e32 v29, v29
	s_waitcnt vmcnt(0)
	v_mul_f32_e32 v24, v37, v24
	v_mul_f32_e32 v24, v24, v46
	v_mul_f32_e32 v25, v25, v48
	v_add_f32_e32 v29, 1.0, v29
	v_rcp_f32_e32 v29, v29
	v_lshlrev_b32_e32 v52, 16, v49
	v_mul_f32_e32 v26, v34, v26
	v_and_b32_e32 v47, 0xffff0000, v47
	v_mul_f32_e32 v24, v29, v24
	v_mul_f32_e32 v29, 0xbfb8aa3b, v48
	v_exp_f32_e32 v29, v29
	v_mul_f32_e32 v26, v26, v52
	v_and_b32_e32 v49, 0xffff0000, v49
	v_mul_f32_e32 v28, v36, v28
	v_add_f32_e32 v29, 1.0, v29
	v_rcp_f32_e32 v29, v29
	v_mul_f32_e32 v36, 0xbfb8aa3b, v45
	v_exp_f32_e32 v36, v36
	v_mul_f32_e32 v27, v35, v27
	v_mul_f32_e32 v29, v29, v25
	v_mul_f32_e32 v25, v30, v44
	v_mul_f32_e32 v30, 0xbfb8aa3b, v50
	v_exp_f32_e32 v30, v30
	v_mul_f32_e32 v25, v38, v25
	v_mul_f32_e32 v25, v25, v50
	v_add_f32_e32 v36, 1.0, v36
	v_add_f32_e32 v30, 1.0, v30
	v_rcp_f32_e32 v30, v30
	v_rcp_f32_e32 v36, v36
	v_mul_f32_e32 v28, v28, v45
	v_mul_f32_e32 v27, v27, v49
	v_mul_f32_e32 v25, v30, v25
	v_mul_f32_e32 v30, 0xbfb8aa3b, v52
	v_exp_f32_e32 v30, v30
	v_mul_f32_e32 v28, v36, v28
	v_cvt_pk_bf16_f32 v24, v28, v24
	v_add_f32_e32 v30, 1.0, v30
	v_rcp_f32_e32 v30, v30
	s_nop 0
	v_mul_f32_e32 v30, v30, v26
	v_mul_f32_e32 v26, v31, v44
	v_mul_f32_e32 v31, 0xbfb8aa3b, v47
	v_exp_f32_e32 v31, v31
	v_mul_f32_e32 v26, v39, v26
	v_mul_f32_e32 v26, v26, v47
	v_add_f32_e32 v31, 1.0, v31
	v_rcp_f32_e32 v31, v31
	s_nop 0
	v_mul_f32_e32 v26, v31, v26
	v_mul_f32_e32 v31, 0xbfb8aa3b, v49
	v_exp_f32_e32 v31, v31
	v_cvt_pk_bf16_f32 v25, v25, v26
	v_cvt_pk_bf16_f32 v26, v32, v29
	v_lshl_add_u64 v[32:33], v[42:43], 0, v[138:139]
	v_add_f32_e32 v31, 1.0, v31
	v_rcp_f32_e32 v31, v31
	s_nop 0
	v_mul_f32_e32 v27, v31, v27
	v_cvt_pk_bf16_f32 v27, v30, v27
	global_store_dwordx4 v[32:33], v[24:27], off
	global_load_dwordx4 v[34:37], v[40:41], off offset:256 nt
	s_nop 0
	global_load_dwordx4 v[24:27], v[136:137], off offset:528
	global_load_dwordx4 v[28:31], v[136:137], off offset:512
	s_waitcnt vmcnt(2)
	v_lshlrev_b32_e32 v42, 16, v36
	s_waitcnt vmcnt(1)
	v_mul_f32_e32 v16, v16, v24
	v_mul_f32_e32 v24, 0xbfb8aa3b, v42
	v_exp_f32_e32 v24, v24
	v_lshlrev_b32_e32 v38, 16, v34
	v_and_b32_e32 v34, 0xffff0000, v34
	v_mul_f32_e32 v16, v16, v42
	v_add_f32_e32 v24, 1.0, v24
	v_rcp_f32_e32 v24, v24
	v_and_b32_e32 v36, 0xffff0000, v36
	v_mul_f32_e32 v17, v17, v25
	v_lshlrev_b32_e32 v39, 16, v35
	v_mul_f32_e32 v24, v16, v24
	v_mul_f32_e32 v16, v21, v44
	v_mul_f32_e32 v21, 0xbfb8aa3b, v34
	v_exp_f32_e32 v21, v21
	s_waitcnt vmcnt(0)
	v_mul_f32_e32 v16, v16, v29
	v_mul_f32_e32 v16, v16, v34
	v_mul_f32_e32 v17, v17, v36
	v_add_f32_e32 v21, 1.0, v21
	v_rcp_f32_e32 v21, v21
	v_lshlrev_b32_e32 v43, 16, v37
	v_mul_f32_e32 v18, v18, v26
	v_and_b32_e32 v35, 0xffff0000, v35
	v_mul_f32_e32 v16, v16, v21
	v_mul_f32_e32 v21, 0xbfb8aa3b, v36
	v_exp_f32_e32 v21, v21
	v_mul_f32_e32 v18, v18, v43
	v_and_b32_e32 v37, 0xffff0000, v37
	v_mul_f32_e32 v20, v20, v28
	v_add_f32_e32 v21, 1.0, v21
	v_rcp_f32_e32 v21, v21
	v_mul_f32_e32 v28, 0xbfb8aa3b, v38
	v_exp_f32_e32 v28, v28
	v_mul_f32_e32 v19, v19, v27
	v_mul_f32_e32 v21, v17, v21
	v_mul_f32_e32 v17, v22, v44
	v_mul_f32_e32 v22, 0xbfb8aa3b, v39
	v_exp_f32_e32 v22, v22
	v_mul_f32_e32 v17, v17, v30
	v_mul_f32_e32 v17, v17, v39
	v_add_f32_e32 v28, 1.0, v28
	v_add_f32_e32 v22, 1.0, v22
	v_rcp_f32_e32 v22, v22
	v_rcp_f32_e32 v28, v28
	v_mul_f32_e32 v19, v19, v37
	v_mul_f32_e32 v20, v20, v38
	v_mul_f32_e32 v17, v17, v22
	v_mul_f32_e32 v22, 0xbfb8aa3b, v43
	v_exp_f32_e32 v22, v22
	v_mul_f32_e32 v20, v20, v28
	v_cvt_pk_bf16_f32 v16, v20, v16
	v_add_f32_e32 v22, 1.0, v22
	v_rcp_f32_e32 v22, v22
	s_nop 0
	v_mul_f32_e32 v22, v18, v22
	v_mul_f32_e32 v18, v23, v44
	v_mul_f32_e32 v23, 0xbfb8aa3b, v35
	v_exp_f32_e32 v23, v23
	v_mul_f32_e32 v18, v18, v31
	v_mul_f32_e32 v18, v18, v35
	v_add_f32_e32 v23, 1.0, v23
	v_rcp_f32_e32 v23, v23
	s_nop 0
	v_mul_f32_e32 v18, v18, v23
	v_mul_f32_e32 v23, 0xbfb8aa3b, v37
	v_exp_f32_e32 v23, v23
	v_cvt_pk_bf16_f32 v17, v17, v18
	v_cvt_pk_bf16_f32 v18, v24, v21
	s_nop 0
	v_add_f32_e32 v23, 1.0, v23
	v_rcp_f32_e32 v23, v23
	s_nop 0
	v_mul_f32_e32 v19, v19, v23
	v_cvt_pk_bf16_f32 v19, v22, v19
	global_store_dwordx4 v[32:33], v[16:19], off offset:256
	global_load_dwordx4 v[24:27], v[40:41], off offset:512 nt
	s_nop 0
	global_load_dwordx4 v[16:19], v[136:137], off offset:1040
	global_load_dwordx4 v[20:23], v[136:137], off offset:1024
	s_waitcnt vmcnt(2)
	v_lshlrev_b32_e32 v30, 16, v26
	s_waitcnt vmcnt(1)
	v_mul_f32_e32 v8, v8, v16
	v_mul_f32_e32 v16, 0xbfb8aa3b, v30
	v_exp_f32_e32 v16, v16
	v_lshlrev_b32_e32 v28, 16, v24
	v_and_b32_e32 v24, 0xffff0000, v24
	v_mul_f32_e32 v8, v8, v30
	v_add_f32_e32 v16, 1.0, v16
	v_rcp_f32_e32 v16, v16
	v_and_b32_e32 v26, 0xffff0000, v26
	v_mul_f32_e32 v9, v9, v17
	v_lshlrev_b32_e32 v29, 16, v25
	v_mul_f32_e32 v16, v8, v16
	v_mul_f32_e32 v8, v13, v44
	v_mul_f32_e32 v13, 0xbfb8aa3b, v24
	v_exp_f32_e32 v13, v13
	s_waitcnt vmcnt(0)
	v_mul_f32_e32 v8, v8, v21
	v_mul_f32_e32 v8, v8, v24
	v_mul_f32_e32 v9, v9, v26
	v_add_f32_e32 v13, 1.0, v13
	v_rcp_f32_e32 v13, v13
	v_lshlrev_b32_e32 v31, 16, v27
	v_mul_f32_e32 v10, v10, v18
	v_and_b32_e32 v25, 0xffff0000, v25
	v_mul_f32_e32 v8, v8, v13
	v_mul_f32_e32 v13, 0xbfb8aa3b, v26
	v_exp_f32_e32 v13, v13
	v_mul_f32_e32 v10, v10, v31
	v_and_b32_e32 v27, 0xffff0000, v27
	v_mul_f32_e32 v12, v12, v20
	v_add_f32_e32 v13, 1.0, v13
	v_rcp_f32_e32 v13, v13
	v_mul_f32_e32 v20, 0xbfb8aa3b, v28
	v_exp_f32_e32 v20, v20
	v_mul_f32_e32 v11, v11, v19
	v_mul_f32_e32 v13, v9, v13
	v_mul_f32_e32 v9, v14, v44
	v_mul_f32_e32 v14, 0xbfb8aa3b, v29
	v_exp_f32_e32 v14, v14
	v_mul_f32_e32 v9, v9, v22
	v_mul_f32_e32 v9, v9, v29
	v_add_f32_e32 v20, 1.0, v20
	v_add_f32_e32 v14, 1.0, v14
	v_rcp_f32_e32 v14, v14
	v_rcp_f32_e32 v20, v20
	v_mul_f32_e32 v11, v11, v27
	v_mul_f32_e32 v12, v12, v28
	v_mul_f32_e32 v9, v9, v14
	v_mul_f32_e32 v14, 0xbfb8aa3b, v31
	v_exp_f32_e32 v14, v14
	v_mul_f32_e32 v12, v12, v20
	v_cvt_pk_bf16_f32 v8, v12, v8
	v_add_f32_e32 v14, 1.0, v14
	v_rcp_f32_e32 v14, v14
	s_nop 0
	v_mul_f32_e32 v14, v10, v14
	v_mul_f32_e32 v10, v15, v44
	v_mul_f32_e32 v15, 0xbfb8aa3b, v25
	v_exp_f32_e32 v15, v15
	v_mul_f32_e32 v10, v10, v23
	v_mul_f32_e32 v10, v10, v25
	v_add_f32_e32 v15, 1.0, v15
	v_rcp_f32_e32 v15, v15
	s_nop 0
	v_mul_f32_e32 v10, v10, v15
	v_mul_f32_e32 v15, 0xbfb8aa3b, v27
	v_exp_f32_e32 v15, v15
	v_cvt_pk_bf16_f32 v9, v9, v10
	v_cvt_pk_bf16_f32 v10, v16, v13
	s_nop 0
	v_add_f32_e32 v15, 1.0, v15
	v_rcp_f32_e32 v15, v15
	s_nop 0
	v_mul_f32_e32 v11, v11, v15
	v_cvt_pk_bf16_f32 v11, v14, v11
	global_store_dwordx4 v[32:33], v[8:11], off offset:512
	global_load_dwordx4 v[16:19], v[40:41], off offset:768 nt
	s_nop 0
	global_load_dwordx4 v[8:11], v[136:137], off offset:1552
	global_load_dwordx4 v[12:15], v[136:137], off offset:1536
	s_waitcnt vmcnt(2)
	v_lshlrev_b32_e32 v22, 16, v18
	s_waitcnt vmcnt(1)
	v_mul_f32_e32 v0, v0, v8
	v_mul_f32_e32 v8, 0xbfb8aa3b, v22
	v_exp_f32_e32 v8, v8
	v_lshlrev_b32_e32 v20, 16, v16
	v_and_b32_e32 v16, 0xffff0000, v16
	v_mul_f32_e32 v0, v0, v22
	v_add_f32_e32 v8, 1.0, v8
	v_rcp_f32_e32 v8, v8
	v_and_b32_e32 v18, 0xffff0000, v18
	v_mul_f32_e32 v1, v1, v9
	v_lshlrev_b32_e32 v21, 16, v17
	v_mul_f32_e32 v8, v0, v8
	v_mul_f32_e32 v0, v5, v44
	v_mul_f32_e32 v5, 0xbfb8aa3b, v16
	v_exp_f32_e32 v5, v5
	s_waitcnt vmcnt(0)
	v_mul_f32_e32 v0, v0, v13
	v_mul_f32_e32 v0, v0, v16
	v_mul_f32_e32 v1, v1, v18
	v_add_f32_e32 v5, 1.0, v5
	v_rcp_f32_e32 v5, v5
	v_lshlrev_b32_e32 v23, 16, v19
	v_mul_f32_e32 v2, v2, v10
	v_and_b32_e32 v17, 0xffff0000, v17
	v_mul_f32_e32 v0, v0, v5
	v_mul_f32_e32 v5, 0xbfb8aa3b, v18
	v_exp_f32_e32 v5, v5
	v_mul_f32_e32 v2, v2, v23
	v_and_b32_e32 v19, 0xffff0000, v19
	v_mul_f32_e32 v4, v4, v12
	v_add_f32_e32 v5, 1.0, v5
	v_rcp_f32_e32 v5, v5
	v_mul_f32_e32 v12, 0xbfb8aa3b, v20
	v_exp_f32_e32 v12, v12
	v_mul_f32_e32 v3, v3, v11
	v_mul_f32_e32 v5, v1, v5
	v_mul_f32_e32 v1, v6, v44
	v_mul_f32_e32 v6, 0xbfb8aa3b, v21
	v_exp_f32_e32 v6, v6
	v_mul_f32_e32 v1, v1, v14
	v_mul_f32_e32 v1, v1, v21
	v_add_f32_e32 v12, 1.0, v12
	v_add_f32_e32 v6, 1.0, v6
	v_rcp_f32_e32 v6, v6
	v_rcp_f32_e32 v12, v12
	v_mul_f32_e32 v3, v3, v19
	v_mul_f32_e32 v4, v4, v20
	v_mul_f32_e32 v1, v1, v6
	v_mul_f32_e32 v6, 0xbfb8aa3b, v23
	v_exp_f32_e32 v6, v6
	v_mul_f32_e32 v4, v4, v12
	v_cvt_pk_bf16_f32 v0, v4, v0
	v_add_f32_e32 v6, 1.0, v6
	v_rcp_f32_e32 v6, v6
	s_nop 0
	v_mul_f32_e32 v6, v2, v6
	v_mul_f32_e32 v2, v7, v44
	v_mul_f32_e32 v7, 0xbfb8aa3b, v17
	v_exp_f32_e32 v7, v7
	v_mul_f32_e32 v2, v2, v15
	v_mul_f32_e32 v2, v2, v17
	v_add_f32_e32 v7, 1.0, v7
	v_rcp_f32_e32 v7, v7
	s_nop 0
	v_mul_f32_e32 v2, v2, v7
	v_mul_f32_e32 v7, 0xbfb8aa3b, v19
	v_exp_f32_e32 v7, v7
	v_cvt_pk_bf16_f32 v1, v1, v2
	v_cvt_pk_bf16_f32 v2, v8, v5
	s_nop 0
	v_add_f32_e32 v7, 1.0, v7
	v_rcp_f32_e32 v7, v7
	s_nop 0
	v_mul_f32_e32 v3, v3, v7
	v_cvt_pk_bf16_f32 v3, v6, v3
	global_store_dwordx4 v[32:33], v[0:3], off offset:768
	s_waitcnt vmcnt(0)
	s_barrier
	s_cbranch_vccnz .LBB0_511

.LBB0_594:
	s_or_b64 exec, exec, s[0:1]
	v_and_or_b32 v14, v0, 15, s9
	v_ashrrev_i32_e32 v0, 1, v0
	v_and_b32_e32 v0, -8, v0
	s_add_i32 s0, 0, 0x22100
	v_add_u32_e32 v8, s24, v0
	v_lshl_add_u32 v0, v14, 4, s0
	s_waitcnt lgkmcnt(0)
	s_barrier
	s_waitcnt lgkmcnt(0)
	ds_read_b128 v[0:3], v0
	s_or_b32 s20, s16, s12
	s_mov_b32 s21, s17
	v_ashrrev_i32_e32 v15, 31, v14
	v_ashrrev_i32_e32 v9, 31, v8
	s_waitcnt lgkmcnt(0)
	v_mov_b32_e32 v4, v1
	v_mov_b32_e32 v5, v2
	v_mov_b32_e32 v1, v3
	v_pk_add_f32 v[0:1], v[4:5], v[0:1]
	v_readlane_b32 s2, v252, 19
	v_add_f32_e32 v0, v0, v1
	v_fmamk_f32 v0, v0, 0x3b000000, v189
	v_rsq_f32_e32 v20, v0
	v_lshl_add_u64 v[0:1], s[20:21], 0, v[14:15]
	v_lshlrev_b64 v[2:3], 12, v[0:1]
	v_lshlrev_b64 v[0:1], 13, v[0:1]
	v_lshl_add_u64 v[0:1], s[66:67], 0, v[0:1]
	v_lshlrev_b64 v[10:11], 1, v[8:9]
	v_readlane_b32 s3, v252, 20
	v_lshl_add_u64 v[16:17], v[0:1], 0, v[10:11]
	v_lshl_add_u64 v[18:19], s[34:35], 0, v[2:3]
	v_lshl_add_u64 v[12:13], v[8:9], 2, s[2:3]
	s_nop 0
	s_nop 0
	global_load_dwordx4 v[212:215], v[16:17], off nt
	global_load_dwordx4 v[224:227], v[12:13], off offset:16
	global_load_dwordx4 v[228:231], v[12:13], off
	global_load_dwordx4 v[216:219], v[16:17], off offset:256 nt
	global_load_dwordx4 v[232:235], v[12:13], off offset:528
	global_load_dwordx4 v[236:239], v[12:13], off offset:512
	global_load_dwordx4 v[174:177], v[16:17], off offset:512 nt
	global_load_dwordx4 v[240:243], v[12:13], off offset:1040
	global_load_dwordx4 v[244:247], v[12:13], off offset:1024
	global_load_dwordx4 v[178:181], v[16:17], off offset:768 nt
	global_load_dwordx4 v[204:207], v[12:13], off offset:1552
	global_load_dwordx4 v[208:211], v[12:13], off offset:1536
	v_mul_f32_e32 v28, v156, v20
	v_mul_f32_e32 v132, v132, v20
	s_and_b64 vcc, exec, s[18:19]
	s_waitcnt vmcnt(9)
	v_lshlrev_b32_e32 v15, 16, v212
	s_nop 0
	v_mul_f32_e32 v4, v228, v28
	v_mul_f32_e32 v4, v4, v15
	v_mul_f32_e32 v15, 0xbfb8aa3b, v15
	v_exp_f32_e32 v15, v15
	v_lshlrev_b32_e32 v26, 16, v214
	v_and_b32_e32 v21, 0xffff0000, v212
	v_and_b32_e32 v24, 0xffff0000, v214
	v_add_f32_e32 v15, 1.0, v15
	v_rcp_f32_e32 v15, v15
	v_lshlrev_b32_e32 v22, 16, v213
	v_lshlrev_b32_e32 v27, 16, v215
	v_and_b32_e32 v23, 0xffff0000, v213
	v_mul_f32_e32 v4, v15, v4
	v_mul_f32_e32 v15, v152, v20
	v_mul_f32_e32 v0, v224, v15
	v_mul_f32_e32 v15, 0xbfb8aa3b, v26
	v_exp_f32_e32 v15, v15
	v_mul_f32_e32 v0, v0, v26
	v_and_b32_e32 v25, 0xffff0000, v215
	v_add_f32_e32 v15, 1.0, v15
	v_rcp_f32_e32 v15, v15
	s_nop 0
	v_mul_f32_e32 v15, v15, v0
	v_mul_f32_e32 v0, v157, v20
	v_mul_f32_e32 v0, v229, v0
	v_mul_f32_e32 v5, 0xbfb8aa3b, v21
	v_exp_f32_e32 v5, v5
	v_mul_f32_e32 v0, v0, v21
	v_add_f32_e32 v5, 1.0, v5
	v_rcp_f32_e32 v5, v5
	s_nop 0
	v_mul_f32_e32 v5, v5, v0
	v_mul_f32_e32 v0, v153, v20
	v_mul_f32_e32 v0, v225, v0
	v_mul_f32_e32 v1, 0xbfb8aa3b, v24
	v_exp_f32_e32 v1, v1
	v_mul_f32_e32 v0, v0, v24
	v_add_f32_e32 v1, 1.0, v1
	v_rcp_f32_e32 v1, v1
	s_nop 0
	v_mul_f32_e32 v21, v1, v0
	v_mul_f32_e32 v1, 0xbfb8aa3b, v22
	v_exp_f32_e32 v1, v1
	v_mul_f32_e32 v0, v158, v20
	v_mul_f32_e32 v0, v230, v0
	v_mul_f32_e32 v0, v0, v22
	v_add_f32_e32 v1, 1.0, v1
	v_rcp_f32_e32 v1, v1
	v_mul_f32_e32 v6, 0xbfb8aa3b, v23
	v_exp_f32_e32 v6, v6
	v_mul_f32_e32 v1, v1, v0
	v_mul_f32_e32 v0, v154, v20
	v_mul_f32_e32 v0, v226, v0
	v_mul_f32_e32 v2, 0xbfb8aa3b, v27
	v_exp_f32_e32 v2, v2
	v_add_f32_e32 v6, 1.0, v6
	v_mul_f32_e32 v0, v0, v27
	v_rcp_f32_e32 v6, v6
	v_add_f32_e32 v2, 1.0, v2
	v_rcp_f32_e32 v2, v2
	s_nop 0
	v_mul_f32_e32 v2, v2, v0
	v_mul_f32_e32 v0, v159, v20
	v_mul_f32_e32 v0, v231, v0
	v_mul_f32_e32 v0, v0, v23
	v_mul_f32_e32 v6, v6, v0
	v_mul_f32_e32 v0, v155, v20
	v_mul_f32_e32 v0, v227, v0
	v_mul_f32_e32 v3, 0xbfb8aa3b, v25
	v_exp_f32_e32 v3, v3
	v_mul_f32_e32 v0, v0, v25
	v_add_f32_e32 v3, 1.0, v3
	v_rcp_f32_e32 v3, v3
	s_nop 0
	v_mul_f32_e32 v3, v3, v0
	v_mov_b32_e32 v0, 0
	v_cvt_pk_fp8_f32 v0, v4, v5
	v_cvt_pk_fp8_f32 v0, v1, v6 op_sel:[0,0,1]
	v_mov_b32_e32 v1, 0
	v_cvt_pk_fp8_f32 v1, v15, v21
	v_lshl_add_u64 v[6:7], v[18:19], 0, v[8:9]
	v_cvt_pk_fp8_f32 v1, v2, v3 op_sel:[0,0,1]
	global_store_dwordx2 v[6:7], v[0:1], off
	s_nop 0
	v_add_u32_e32 v0, 0x80, v8
	v_ashrrev_i32_e32 v1, 31, v0
	v_lshl_add_u64 v[0:1], v[0:1], 2, s[2:3]
	s_nop 0
	s_nop 0
	s_waitcnt vmcnt(7)
	v_lshlrev_b32_e32 v15, 16, v216
	v_lshlrev_b32_e32 v30, 16, v219
	v_and_b32_e32 v31, 0xffff0000, v219
	v_mul_f32_e32 v5, 0xbfb8aa3b, v15
	v_exp_f32_e32 v5, v5
	v_lshlrev_b32_e32 v19, 16, v218
	v_and_b32_e32 v21, 0xffff0000, v218
	v_mul_f32_e32 v4, v148, v20
	v_add_f32_e32 v5, 1.0, v5
	v_rcp_f32_e32 v5, v5
	s_nop 0
	v_mul_f32_e32 v4, v4, v236
	v_mul_f32_e32 v4, v4, v15
	v_and_b32_e32 v2, 0xffff0000, v216
	v_mul_f32_e32 v26, v4, v5
	v_mul_f32_e32 v5, 0xbfb8aa3b, v19
	v_exp_f32_e32 v5, v5
	v_mul_f32_e32 v4, v144, v20
	v_mul_f32_e32 v4, v4, v232
	v_mul_f32_e32 v4, v4, v19
	v_add_f32_e32 v5, 1.0, v5
	v_rcp_f32_e32 v5, v5
	v_lshlrev_b32_e32 v18, 16, v217
	v_mul_f32_e32 v15, 0xbfb8aa3b, v18
	v_exp_f32_e32 v15, v15
	v_mul_f32_e32 v4, v4, v5
	v_mul_f32_e32 v5, v149, v20
	v_mul_f32_e32 v5, v5, v237
	v_mul_f32_e32 v5, v5, v2
	v_mul_f32_e32 v2, 0xbfb8aa3b, v2
	v_exp_f32_e32 v2, v2
	v_add_f32_e32 v15, 1.0, v15
	v_rcp_f32_e32 v15, v15
	v_and_b32_e32 v3, 0xffff0000, v217
	v_add_f32_e32 v2, 1.0, v2
	v_rcp_f32_e32 v2, v2
	s_nop 0
	v_mul_f32_e32 v19, v5, v2
	v_mul_f32_e32 v5, 0xbfb8aa3b, v21
	v_exp_f32_e32 v5, v5
	v_mul_f32_e32 v2, v145, v20
	v_mul_f32_e32 v2, v2, v233
	v_mul_f32_e32 v2, v2, v21
	v_add_f32_e32 v5, 1.0, v5
	v_rcp_f32_e32 v5, v5
	s_nop 0
	v_mul_f32_e32 v5, v2, v5
	v_mul_f32_e32 v2, v150, v20
	v_mul_f32_e32 v2, v2, v238
	v_mul_f32_e32 v2, v2, v18
	v_mul_f32_e32 v21, v2, v15
	v_mul_f32_e32 v15, 0xbfb8aa3b, v30
	v_exp_f32_e32 v15, v15
	v_mul_f32_e32 v2, v146, v20
	v_mul_f32_e32 v2, v2, v234
	v_mul_f32_e32 v2, v2, v30
	v_add_f32_e32 v15, 1.0, v15
	v_rcp_f32_e32 v15, v15
	v_mul_f32_e32 v18, 0xbfb8aa3b, v31
	v_exp_f32_e32 v18, v18
	v_mul_f32_e32 v15, v2, v15
	v_mul_f32_e32 v2, v151, v20
	v_mul_f32_e32 v2, v2, v239
	v_mul_f32_e32 v2, v2, v3
	v_mul_f32_e32 v3, 0xbfb8aa3b, v3
	v_exp_f32_e32 v3, v3
	v_add_f32_e32 v18, 1.0, v18
	v_rcp_f32_e32 v18, v18
	v_add_f32_e32 v3, 1.0, v3
	v_rcp_f32_e32 v3, v3
	s_nop 0
	v_mul_f32_e32 v3, v2, v3
	v_mul_f32_e32 v2, v147, v20
	v_mul_f32_e32 v2, v2, v235
	v_mul_f32_e32 v2, v2, v31
	v_mul_f32_e32 v18, v2, v18
	v_mov_b32_e32 v2, 0
	v_cvt_pk_fp8_f32 v2, v26, v19
	v_cvt_pk_fp8_f32 v2, v21, v3 op_sel:[0,0,1]
	v_mov_b32_e32 v3, 0
	v_cvt_pk_fp8_f32 v3, v4, v5
	v_cvt_pk_fp8_f32 v3, v15, v18 op_sel:[0,0,1]
	global_store_dwordx2 v[6:7], v[2:3], off offset:128
	v_add_u32_e32 v2, 0x100, v8
	v_ashrrev_i32_e32 v3, 31, v2
	s_nop 0
	v_lshl_add_u64 v[2:3], v[2:3], 2, s[2:3]
	s_nop 0
	s_nop 0
	s_waitcnt vmcnt(5)
	v_lshlrev_b32_e32 v15, 16, v176
	v_and_b32_e32 v18, 0xffff0000, v176
	v_mul_f32_e32 v24, v140, v20
	v_lshlrev_b32_e32 v4, 16, v174
	s_nop 0
	v_mul_f32_e32 v24, v24, v244
	v_mul_f32_e32 v24, v24, v4
	v_mul_f32_e32 v4, 0xbfb8aa3b, v4
	v_exp_f32_e32 v4, v4
	v_and_b32_e32 v5, 0xffff0000, v174
	v_lshlrev_b32_e32 v19, 16, v175
	v_lshlrev_b32_e32 v22, 16, v177
	v_add_f32_e32 v4, 1.0, v4
	v_rcp_f32_e32 v4, v4
	v_and_b32_e32 v21, 0xffff0000, v175
	v_and_b32_e32 v23, 0xffff0000, v177
	v_mul_f32_e32 v24, v24, v4
	v_mul_f32_e32 v4, v136, v20
	v_mul_f32_e32 v4, v4, v240
	v_mul_f32_e32 v4, v4, v15
	v_mul_f32_e32 v15, 0xbfb8aa3b, v15
	v_exp_f32_e32 v15, v15
	s_nop 0
	v_add_f32_e32 v15, 1.0, v15
	v_rcp_f32_e32 v15, v15
	s_nop 0
	v_mul_f32_e32 v15, v4, v15
	v_mul_f32_e32 v4, v141, v20
	v_mul_f32_e32 v4, v4, v245
	v_mul_f32_e32 v4, v4, v5
	v_mul_f32_e32 v5, 0xbfb8aa3b, v5
	v_exp_f32_e32 v5, v5
	s_nop 0
	v_add_f32_e32 v5, 1.0, v5
	v_rcp_f32_e32 v5, v5
	s_nop 0
	v_mul_f32_e32 v5, v4, v5
	v_mul_f32_e32 v4, v137, v20
	v_mul_f32_e32 v4, v4, v241
	v_mul_f32_e32 v4, v4, v18
	v_mul_f32_e32 v18, 0xbfb8aa3b, v18
	v_exp_f32_e32 v18, v18
	s_nop 0
	v_add_f32_e32 v18, 1.0, v18
	v_rcp_f32_e32 v18, v18
	s_nop 0
	v_mul_f32_e32 v18, v4, v18
	v_mul_f32_e32 v4, v142, v20
	v_mul_f32_e32 v4, v4, v246
	v_mul_f32_e32 v4, v4, v19
	v_mul_f32_e32 v19, 0xbfb8aa3b, v19
	v_exp_f32_e32 v19, v19
	s_nop 0
	v_add_f32_e32 v19, 1.0, v19
	v_rcp_f32_e32 v19, v19
	s_nop 0
	v_mul_f32_e32 v25, v4, v19
	v_mul_f32_e32 v19, 0xbfb8aa3b, v22
	v_exp_f32_e32 v19, v19
	v_mul_f32_e32 v4, v138, v20
	v_mul_f32_e32 v4, v4, v242
	v_mul_f32_e32 v4, v4, v22
	v_add_f32_e32 v19, 1.0, v19
	v_rcp_f32_e32 v19, v19
	s_nop 0
	v_mul_f32_e32 v19, v4, v19
	v_mul_f32_e32 v4, v143, v20
	v_mul_f32_e32 v4, v4, v247
	v_mul_f32_e32 v4, v4, v21
	v_mul_f32_e32 v21, 0xbfb8aa3b, v21
	v_exp_f32_e32 v21, v21
	s_nop 0
	v_add_f32_e32 v21, 1.0, v21
	v_rcp_f32_e32 v21, v21
	s_nop 0
	v_mul_f32_e32 v22, v4, v21
	v_mul_f32_e32 v21, 0xbfb8aa3b, v23
	v_exp_f32_e32 v21, v21
	v_mul_f32_e32 v4, v139, v20
	v_mul_f32_e32 v4, v4, v243
	v_mul_f32_e32 v4, v4, v23
	v_add_f32_e32 v21, 1.0, v21
	v_rcp_f32_e32 v21, v21
	s_nop 0
	v_mul_f32_e32 v21, v4, v21
	v_mov_b32_e32 v4, 0
	v_cvt_pk_fp8_f32 v4, v24, v5
	v_mov_b32_e32 v5, 0
	v_cvt_pk_fp8_f32 v5, v15, v18
	v_cvt_pk_fp8_f32 v4, v25, v22 op_sel:[0,0,1]
	v_cvt_pk_fp8_f32 v5, v19, v21 op_sel:[0,0,1]
	global_store_dwordx2 v[6:7], v[4:5], off offset:256
	v_add_u32_e32 v4, 0x180, v8
	v_ashrrev_i32_e32 v5, 31, v4
	v_lshl_add_u64 v[4:5], v[4:5], 2, s[2:3]
	s_nop 0
	s_nop 0
	s_nop 0
	s_nop 0
	s_waitcnt vmcnt(3)
	v_lshlrev_b32_e32 v15, 16, v178
	s_nop 0
	v_mul_f32_e32 v26, v132, v208
	v_mul_f32_e32 v26, v26, v15
	v_mul_f32_e32 v15, 0xbfb8aa3b, v15
	v_exp_f32_e32 v15, v15
	v_lshlrev_b32_e32 v30, 16, v180
	v_and_b32_e32 v16, 0xffff0000, v178
	v_and_b32_e32 v18, 0xffff0000, v180
	v_add_f32_e32 v15, 1.0, v15
	v_rcp_f32_e32 v15, v15
	v_lshlrev_b32_e32 v21, 16, v179
	v_lshlrev_b32_e32 v31, 16, v181
	v_and_b32_e32 v17, 0xffff0000, v179
	v_mul_f32_e32 v15, v26, v15
	v_mul_f32_e32 v26, v128, v20
	v_mul_f32_e32 v22, v26, v204
	v_mul_f32_e32 v26, 0xbfb8aa3b, v30
	v_exp_f32_e32 v26, v26
	v_mul_f32_e32 v22, v22, v30
	v_and_b32_e32 v19, 0xffff0000, v181
	v_add_f32_e32 v26, 1.0, v26
	v_rcp_f32_e32 v26, v26
	s_nop 0
	v_mul_f32_e32 v22, v22, v26
	v_mul_f32_e32 v26, v133, v20
	v_mul_f32_e32 v26, v26, v209
	v_mul_f32_e32 v26, v26, v16
	v_mul_f32_e32 v16, 0xbfb8aa3b, v16
	v_exp_f32_e32 v16, v16
	s_nop 0
	v_add_f32_e32 v16, 1.0, v16
	v_rcp_f32_e32 v16, v16
	s_nop 0
	v_mul_f32_e32 v26, v26, v16
	v_mul_f32_e32 v16, v129, v20
	v_mul_f32_e32 v16, v16, v205
	v_mul_f32_e32 v16, v16, v18
	v_mul_f32_e32 v18, 0xbfb8aa3b, v18
	v_exp_f32_e32 v18, v18
	v_mul_f32_e32 v23, 0xbfb8aa3b, v31
	v_exp_f32_e32 v23, v23
	v_add_f32_e32 v18, 1.0, v18
	v_rcp_f32_e32 v18, v18
	v_add_f32_e32 v23, 1.0, v23
	v_rcp_f32_e32 v23, v23
	v_mul_f32_e32 v18, v16, v18
	v_mul_f32_e32 v16, v134, v20
	v_mul_f32_e32 v16, v16, v210
	v_mul_f32_e32 v16, v16, v21
	v_mul_f32_e32 v21, 0xbfb8aa3b, v21
	v_exp_f32_e32 v21, v21
	s_nop 0
	v_add_f32_e32 v21, 1.0, v21
	v_rcp_f32_e32 v21, v21
	s_nop 0
	v_mul_f32_e32 v21, v16, v21
	v_mul_f32_e32 v16, v130, v20
	v_mul_f32_e32 v16, v16, v206
	v_mul_f32_e32 v16, v16, v31
	v_mul_f32_e32 v23, v16, v23
	v_mul_f32_e32 v16, v135, v20
	v_mul_f32_e32 v16, v16, v211
	v_mul_f32_e32 v16, v16, v17
	v_mul_f32_e32 v17, 0xbfb8aa3b, v17
	v_exp_f32_e32 v17, v17
	s_nop 0
	v_add_f32_e32 v17, 1.0, v17
	v_rcp_f32_e32 v17, v17
	s_nop 0
	v_mul_f32_e32 v17, v16, v17
	v_mul_f32_e32 v16, v131, v20
	v_mul_f32_e32 v16, v16, v207
	v_mul_f32_e32 v16, v16, v19
	v_mul_f32_e32 v19, 0xbfb8aa3b, v19
	v_exp_f32_e32 v19, v19
	s_nop 0
	v_add_f32_e32 v19, 1.0, v19
	v_rcp_f32_e32 v19, v19
	s_nop 0
	v_mul_f32_e32 v19, v16, v19
	v_mov_b32_e32 v16, 0
	v_cvt_pk_fp8_f32 v16, v15, v26
	v_cvt_pk_fp8_f32 v16, v21, v17 op_sel:[0,0,1]
	v_mov_b32_e32 v17, 0
	v_cvt_pk_fp8_f32 v17, v22, v18
	v_cvt_pk_fp8_f32 v17, v23, v19 op_sel:[0,0,1]
	global_store_dwordx2 v[6:7], v[16:17], off offset:384
	v_or_b32_e32 v6, 16, v14
	v_lshl_add_u32 v7, v6, 4, s0
	ds_read_b128 v[16:19], v7
	s_waitcnt lgkmcnt(0)
	v_mov_b32_e32 v20, v17
	v_mov_b32_e32 v21, v18
	v_mov_b32_e32 v17, v19
	v_pk_add_f32 v[16:17], v[20:21], v[16:17]
	s_nop 0
	v_add_f32_e32 v7, v16, v17
	v_fmamk_f32 v7, v7, 0x3b000000, v189
	v_rsq_f32_e32 v15, v7
	v_ashrrev_i32_e32 v7, 31, v6
	v_lshl_add_u64 v[16:17], s[20:21], 0, v[6:7]
	v_lshlrev_b64 v[6:7], 12, v[16:17]
	v_lshlrev_b64 v[16:17], 13, v[16:17]
	v_lshl_add_u64 v[18:19], s[66:67], 0, v[16:17]
	v_lshl_add_u64 v[16:17], s[34:35], 0, v[6:7]
	v_lshl_add_u64 v[6:7], v[18:19], 0, v[10:11]
	global_load_dwordx4 v[212:215], v[6:7], off nt
	global_load_dwordx4 v[216:219], v[6:7], off offset:256 nt
	global_load_dwordx4 v[174:177], v[6:7], off offset:512 nt
	global_load_dwordx4 v[178:181], v[6:7], off offset:768 nt
	s_nop 0
	s_nop 0
	v_lshl_add_u64 v[16:17], v[16:17], 0, v[8:9]
	v_mul_f32_e32 v100, v100, v15
	s_waitcnt vmcnt(3)
	v_lshlrev_b32_e32 v30, 16, v212
	v_lshlrev_b32_e32 v130, 16, v215
	v_and_b32_e32 v131, 0xffff0000, v215
	v_mul_f32_e32 v21, 0xbfb8aa3b, v30
	v_exp_f32_e32 v21, v21
	v_lshlrev_b32_e32 v128, 16, v214
	v_and_b32_e32 v129, 0xffff0000, v214
	v_mul_f32_e32 v20, v124, v15
	v_add_f32_e32 v21, 1.0, v21
	v_rcp_f32_e32 v21, v21
	s_nop 0
	v_mul_f32_e32 v20, v228, v20
	v_mul_f32_e32 v20, v20, v30
	v_and_b32_e32 v18, 0xffff0000, v212
	v_mul_f32_e32 v26, v21, v20
	v_mul_f32_e32 v21, 0xbfb8aa3b, v128
	v_exp_f32_e32 v21, v21
	v_mul_f32_e32 v20, v120, v15
	v_mul_f32_e32 v20, v224, v20
	v_mul_f32_e32 v20, v20, v128
	v_add_f32_e32 v21, 1.0, v21
	v_rcp_f32_e32 v21, v21
	v_lshlrev_b32_e32 v31, 16, v213
	v_mul_f32_e32 v22, 0xbfb8aa3b, v31
	v_exp_f32_e32 v22, v22
	v_mul_f32_e32 v20, v21, v20
	v_mul_f32_e32 v21, v125, v15
	v_mul_f32_e32 v21, v229, v21
	v_mul_f32_e32 v21, v21, v18
	v_mul_f32_e32 v18, 0xbfb8aa3b, v18
	v_exp_f32_e32 v18, v18
	v_add_f32_e32 v22, 1.0, v22
	v_rcp_f32_e32 v22, v22
	v_and_b32_e32 v19, 0xffff0000, v213
	v_add_f32_e32 v18, 1.0, v18
	v_rcp_f32_e32 v18, v18
	s_nop 0
	v_mul_f32_e32 v27, v18, v21
	v_mul_f32_e32 v21, 0xbfb8aa3b, v129
	v_exp_f32_e32 v21, v21
	v_mul_f32_e32 v18, v121, v15
	v_mul_f32_e32 v18, v225, v18
	v_mul_f32_e32 v18, v18, v129
	v_add_f32_e32 v21, 1.0, v21
	v_rcp_f32_e32 v21, v21
	v_mul_f32_e32 v23, 0xbfb8aa3b, v131
	v_exp_f32_e32 v23, v23
	v_mul_f32_e32 v21, v21, v18
	v_mul_f32_e32 v18, v126, v15
	v_mul_f32_e32 v18, v230, v18
	v_mul_f32_e32 v18, v18, v31
	v_mul_f32_e32 v28, v22, v18
	v_mul_f32_e32 v22, 0xbfb8aa3b, v130
	v_exp_f32_e32 v22, v22
	v_mul_f32_e32 v18, v122, v15
	v_mul_f32_e32 v18, v226, v18
	v_mul_f32_e32 v18, v18, v130
	v_add_f32_e32 v22, 1.0, v22
	v_rcp_f32_e32 v22, v22
	v_add_f32_e32 v23, 1.0, v23
	v_rcp_f32_e32 v23, v23
	v_mul_f32_e32 v22, v22, v18
	v_mul_f32_e32 v18, v127, v15
	v_mul_f32_e32 v18, v231, v18
	v_mul_f32_e32 v18, v18, v19
	v_mul_f32_e32 v19, 0xbfb8aa3b, v19
	v_exp_f32_e32 v19, v19
	s_nop 0
	v_add_f32_e32 v19, 1.0, v19
	v_rcp_f32_e32 v19, v19
	s_nop 0
	v_mul_f32_e32 v19, v19, v18
	v_mul_f32_e32 v18, v123, v15
	v_mul_f32_e32 v18, v227, v18
	v_mul_f32_e32 v18, v18, v131
	v_mul_f32_e32 v23, v23, v18
	v_mov_b32_e32 v18, 0
	v_cvt_pk_fp8_f32 v18, v26, v27
	v_cvt_pk_fp8_f32 v18, v28, v19 op_sel:[0,0,1]
	v_mov_b32_e32 v19, 0
	v_cvt_pk_fp8_f32 v19, v20, v21
	v_cvt_pk_fp8_f32 v19, v22, v23 op_sel:[0,0,1]
	global_store_dwordx2 v[16:17], v[18:19], off
	s_nop 0
	s_nop 0
	s_nop 0
	s_nop 0
	s_waitcnt vmcnt(3)
	v_lshlrev_b32_e32 v30, 16, v216
	v_lshlrev_b32_e32 v122, 16, v219
	v_and_b32_e32 v123, 0xffff0000, v219
	v_mul_f32_e32 v21, 0xbfb8aa3b, v30
	v_exp_f32_e32 v21, v21
	v_lshlrev_b32_e32 v120, 16, v218
	v_and_b32_e32 v121, 0xffff0000, v218
	v_mul_f32_e32 v20, v116, v15
	v_add_f32_e32 v21, 1.0, v21
	v_rcp_f32_e32 v21, v21
	s_nop 0
	v_mul_f32_e32 v20, v20, v236
	v_mul_f32_e32 v20, v20, v30
	v_and_b32_e32 v18, 0xffff0000, v216
	v_mul_f32_e32 v26, v20, v21
	v_mul_f32_e32 v21, 0xbfb8aa3b, v120
	v_exp_f32_e32 v21, v21
	v_mul_f32_e32 v20, v112, v15
	v_mul_f32_e32 v20, v20, v232
	v_mul_f32_e32 v20, v20, v120
	v_add_f32_e32 v21, 1.0, v21
	v_rcp_f32_e32 v21, v21
	v_lshlrev_b32_e32 v31, 16, v217
	v_mul_f32_e32 v22, 0xbfb8aa3b, v31
	v_exp_f32_e32 v22, v22
	v_mul_f32_e32 v20, v20, v21
	v_mul_f32_e32 v21, v117, v15
	v_mul_f32_e32 v21, v21, v237
	v_mul_f32_e32 v21, v21, v18
	v_mul_f32_e32 v18, 0xbfb8aa3b, v18
	v_exp_f32_e32 v18, v18
	v_add_f32_e32 v22, 1.0, v22
	v_rcp_f32_e32 v22, v22
	v_and_b32_e32 v19, 0xffff0000, v217
	v_add_f32_e32 v18, 1.0, v18
	v_rcp_f32_e32 v18, v18
	s_nop 0
	v_mul_f32_e32 v27, v21, v18
	v_mul_f32_e32 v21, 0xbfb8aa3b, v121
	v_exp_f32_e32 v21, v21
	v_mul_f32_e32 v18, v113, v15
	v_mul_f32_e32 v18, v18, v233
	v_mul_f32_e32 v18, v18, v121
	v_add_f32_e32 v21, 1.0, v21
	v_rcp_f32_e32 v21, v21
	v_mul_f32_e32 v23, 0xbfb8aa3b, v123
	v_exp_f32_e32 v23, v23
	v_mul_f32_e32 v21, v18, v21
	v_mul_f32_e32 v18, v118, v15
	v_mul_f32_e32 v18, v18, v238
	v_mul_f32_e32 v18, v18, v31
	v_mul_f32_e32 v28, v18, v22
	v_mul_f32_e32 v22, 0xbfb8aa3b, v122
	v_exp_f32_e32 v22, v22
	v_mul_f32_e32 v18, v114, v15
	v_mul_f32_e32 v18, v18, v234
	v_mul_f32_e32 v18, v18, v122
	v_add_f32_e32 v22, 1.0, v22
	v_rcp_f32_e32 v22, v22
	v_add_f32_e32 v23, 1.0, v23
	v_rcp_f32_e32 v23, v23
	v_mul_f32_e32 v22, v18, v22
	v_mul_f32_e32 v18, v119, v15
	v_mul_f32_e32 v18, v18, v239
	v_mul_f32_e32 v18, v18, v19
	v_mul_f32_e32 v19, 0xbfb8aa3b, v19
	v_exp_f32_e32 v19, v19
	s_nop 0
	v_add_f32_e32 v19, 1.0, v19
	v_rcp_f32_e32 v19, v19
	s_nop 0
	v_mul_f32_e32 v19, v18, v19
	v_mul_f32_e32 v18, v115, v15
	v_mul_f32_e32 v18, v18, v235
	v_mul_f32_e32 v18, v18, v123
	v_mul_f32_e32 v23, v18, v23
	v_mov_b32_e32 v18, 0
	v_cvt_pk_fp8_f32 v18, v26, v27
	v_cvt_pk_fp8_f32 v18, v28, v19 op_sel:[0,0,1]
	v_mov_b32_e32 v19, 0
	v_cvt_pk_fp8_f32 v19, v20, v21
	v_cvt_pk_fp8_f32 v19, v22, v23 op_sel:[0,0,1]
	global_store_dwordx2 v[16:17], v[18:19], off offset:128
	s_nop 0
	s_nop 0
	s_nop 0
	s_nop 0
	s_waitcnt vmcnt(3)
	v_lshlrev_b32_e32 v30, 16, v174
	v_lshlrev_b32_e32 v114, 16, v177
	v_and_b32_e32 v115, 0xffff0000, v177
	v_mul_f32_e32 v21, 0xbfb8aa3b, v30
	v_exp_f32_e32 v21, v21
	v_lshlrev_b32_e32 v112, 16, v176
	v_and_b32_e32 v113, 0xffff0000, v176
	v_mul_f32_e32 v20, v108, v15
	v_add_f32_e32 v21, 1.0, v21
	v_rcp_f32_e32 v21, v21
	s_nop 0
	v_mul_f32_e32 v20, v20, v244
	v_mul_f32_e32 v20, v20, v30
	v_and_b32_e32 v18, 0xffff0000, v174
	v_mul_f32_e32 v26, v20, v21
	v_mul_f32_e32 v21, 0xbfb8aa3b, v112
	v_exp_f32_e32 v21, v21
	v_mul_f32_e32 v20, v104, v15
	v_mul_f32_e32 v20, v20, v240
	v_mul_f32_e32 v20, v20, v112
	v_add_f32_e32 v21, 1.0, v21
	v_rcp_f32_e32 v21, v21
	v_lshlrev_b32_e32 v31, 16, v175
	v_mul_f32_e32 v22, 0xbfb8aa3b, v31
	v_exp_f32_e32 v22, v22
	v_mul_f32_e32 v20, v20, v21
	v_mul_f32_e32 v21, v109, v15
	v_mul_f32_e32 v21, v21, v245
	v_mul_f32_e32 v21, v21, v18
	v_mul_f32_e32 v18, 0xbfb8aa3b, v18
	v_exp_f32_e32 v18, v18
	v_add_f32_e32 v22, 1.0, v22
	v_rcp_f32_e32 v22, v22
	v_and_b32_e32 v19, 0xffff0000, v175
	v_add_f32_e32 v18, 1.0, v18
	v_rcp_f32_e32 v18, v18
	s_nop 0
	v_mul_f32_e32 v27, v21, v18
	v_mul_f32_e32 v21, 0xbfb8aa3b, v113
	v_exp_f32_e32 v21, v21
	v_mul_f32_e32 v18, v105, v15
	v_mul_f32_e32 v18, v18, v241
	v_mul_f32_e32 v18, v18, v113
	v_add_f32_e32 v21, 1.0, v21
	v_rcp_f32_e32 v21, v21
	v_mul_f32_e32 v23, 0xbfb8aa3b, v115
	v_exp_f32_e32 v23, v23
	v_mul_f32_e32 v21, v18, v21
	v_mul_f32_e32 v18, v110, v15
	v_mul_f32_e32 v18, v18, v246
	v_mul_f32_e32 v18, v18, v31
	v_mul_f32_e32 v28, v18, v22
	v_mul_f32_e32 v22, 0xbfb8aa3b, v114
	v_exp_f32_e32 v22, v22
	v_mul_f32_e32 v18, v106, v15
	v_mul_f32_e32 v18, v18, v242
	v_mul_f32_e32 v18, v18, v114
	v_add_f32_e32 v22, 1.0, v22
	v_rcp_f32_e32 v22, v22
	v_add_f32_e32 v23, 1.0, v23
	v_rcp_f32_e32 v23, v23
	v_mul_f32_e32 v22, v18, v22
	v_mul_f32_e32 v18, v111, v15
	v_mul_f32_e32 v18, v18, v247
	v_mul_f32_e32 v18, v18, v19
	v_mul_f32_e32 v19, 0xbfb8aa3b, v19
	v_exp_f32_e32 v19, v19
	s_nop 0
	v_add_f32_e32 v19, 1.0, v19
	v_rcp_f32_e32 v19, v19
	s_nop 0
	v_mul_f32_e32 v19, v18, v19
	v_mul_f32_e32 v18, v107, v15
	v_mul_f32_e32 v18, v18, v243
	v_mul_f32_e32 v18, v18, v115
	v_mul_f32_e32 v23, v18, v23
	v_mov_b32_e32 v18, 0
	v_cvt_pk_fp8_f32 v18, v26, v27
	v_cvt_pk_fp8_f32 v18, v28, v19 op_sel:[0,0,1]
	v_mov_b32_e32 v19, 0
	v_cvt_pk_fp8_f32 v19, v20, v21
	v_cvt_pk_fp8_f32 v19, v22, v23 op_sel:[0,0,1]
	global_store_dwordx2 v[16:17], v[18:19], off offset:256
	s_nop 0
	s_nop 0
	s_nop 0
	s_nop 0
	s_waitcnt vmcnt(3)
	v_lshlrev_b32_e32 v6, 16, v178
	v_lshlrev_b32_e32 v30, 16, v180
	s_nop 0
	v_mul_f32_e32 v26, v100, v208
	v_mul_f32_e32 v26, v26, v6
	v_mul_f32_e32 v6, 0xbfb8aa3b, v6
	v_exp_f32_e32 v6, v6
	v_and_b32_e32 v7, 0xffff0000, v178
	v_and_b32_e32 v20, 0xffff0000, v180
	v_lshlrev_b32_e32 v18, 16, v179
	v_add_f32_e32 v6, 1.0, v6
	v_rcp_f32_e32 v6, v6
	v_lshlrev_b32_e32 v31, 16, v181
	v_and_b32_e32 v19, 0xffff0000, v179
	v_and_b32_e32 v21, 0xffff0000, v181
	v_mul_f32_e32 v26, v26, v6
	v_mul_f32_e32 v6, v96, v15
	v_mul_f32_e32 v6, v6, v204
	v_mul_f32_e32 v22, 0xbfb8aa3b, v30
	v_exp_f32_e32 v22, v22
	v_mul_f32_e32 v6, v6, v30
	v_add_f32_e32 v22, 1.0, v22
	v_rcp_f32_e32 v22, v22
	s_nop 0
	v_mul_f32_e32 v22, v6, v22
	v_mul_f32_e32 v6, v101, v15
	v_mul_f32_e32 v6, v6, v209
	v_mul_f32_e32 v6, v6, v7
	v_mul_f32_e32 v7, 0xbfb8aa3b, v7
	v_exp_f32_e32 v7, v7
	s_nop 0
	v_add_f32_e32 v7, 1.0, v7
	v_rcp_f32_e32 v7, v7
	s_nop 0
	v_mul_f32_e32 v7, v6, v7
	v_mul_f32_e32 v6, v97, v15
	v_mul_f32_e32 v6, v6, v205
	v_mul_f32_e32 v6, v6, v20
	v_mul_f32_e32 v20, 0xbfb8aa3b, v20
	v_exp_f32_e32 v20, v20
	v_mul_f32_e32 v23, 0xbfb8aa3b, v31
	v_exp_f32_e32 v23, v23
	v_add_f32_e32 v20, 1.0, v20
	v_rcp_f32_e32 v20, v20
	v_add_f32_e32 v23, 1.0, v23
	v_rcp_f32_e32 v23, v23
	v_mul_f32_e32 v20, v6, v20
	v_mul_f32_e32 v6, v102, v15
	v_mul_f32_e32 v6, v6, v210
	v_mul_f32_e32 v6, v6, v18
	v_mul_f32_e32 v18, 0xbfb8aa3b, v18
	v_exp_f32_e32 v18, v18
	s_nop 0
	v_add_f32_e32 v18, 1.0, v18
	v_rcp_f32_e32 v18, v18
	s_nop 0
	v_mul_f32_e32 v18, v6, v18
	v_mul_f32_e32 v6, v98, v15
	v_mul_f32_e32 v6, v6, v206
	v_mul_f32_e32 v6, v6, v31
	v_mul_f32_e32 v23, v6, v23
	v_mul_f32_e32 v6, v103, v15
	v_mul_f32_e32 v6, v6, v211
	v_mul_f32_e32 v6, v6, v19
	v_mul_f32_e32 v19, 0xbfb8aa3b, v19
	v_exp_f32_e32 v19, v19
	s_nop 0
	v_add_f32_e32 v19, 1.0, v19
	v_rcp_f32_e32 v19, v19
	s_nop 0
	v_mul_f32_e32 v19, v6, v19
	v_mul_f32_e32 v6, v99, v15
	v_mul_f32_e32 v15, 0xbfb8aa3b, v21
	v_exp_f32_e32 v15, v15
	v_mul_f32_e32 v6, v6, v207
	v_mul_f32_e32 v6, v6, v21
	v_add_f32_e32 v15, 1.0, v15
	v_rcp_f32_e32 v15, v15
	s_nop 0
	v_mul_f32_e32 v15, v6, v15
	v_mov_b32_e32 v6, 0
	v_cvt_pk_fp8_f32 v6, v26, v7
	v_mov_b32_e32 v7, 0
	v_cvt_pk_fp8_f32 v7, v22, v20
	v_cvt_pk_fp8_f32 v6, v18, v19 op_sel:[0,0,1]
	v_cvt_pk_fp8_f32 v7, v23, v15 op_sel:[0,0,1]
	global_store_dwordx2 v[16:17], v[6:7], off offset:384
	v_or_b32_e32 v6, 32, v14
	v_lshl_add_u32 v7, v6, 4, s0
	ds_read_b128 v[16:19], v7
	s_waitcnt lgkmcnt(0)
	v_mov_b32_e32 v20, v17
	v_mov_b32_e32 v21, v18
	v_mov_b32_e32 v17, v19
	v_pk_add_f32 v[16:17], v[20:21], v[16:17]
	s_nop 0
	v_add_f32_e32 v7, v16, v17
	v_fmamk_f32 v7, v7, 0x3b000000, v189
	v_rsq_f32_e32 v15, v7
	v_ashrrev_i32_e32 v7, 31, v6
	v_lshl_add_u64 v[16:17], s[20:21], 0, v[6:7]
	v_lshlrev_b64 v[6:7], 12, v[16:17]
	v_lshlrev_b64 v[16:17], 13, v[16:17]
	v_lshl_add_u64 v[18:19], s[66:67], 0, v[16:17]
	v_lshl_add_u64 v[16:17], s[34:35], 0, v[6:7]
	v_lshl_add_u64 v[6:7], v[18:19], 0, v[10:11]
	global_load_dwordx4 v[212:215], v[6:7], off nt
	global_load_dwordx4 v[216:219], v[6:7], off offset:256 nt
	global_load_dwordx4 v[174:177], v[6:7], off offset:512 nt
	global_load_dwordx4 v[178:181], v[6:7], off offset:768 nt
	s_nop 0
	s_nop 0
	v_lshl_add_u64 v[16:17], v[16:17], 0, v[8:9]
	v_mul_f32_e32 v68, v68, v15
	s_waitcnt vmcnt(3)
	v_lshlrev_b32_e32 v30, 16, v212
	v_lshlrev_b32_e32 v98, 16, v215
	v_and_b32_e32 v99, 0xffff0000, v215
	v_mul_f32_e32 v21, 0xbfb8aa3b, v30
	v_exp_f32_e32 v21, v21
	v_lshlrev_b32_e32 v96, 16, v214
	v_and_b32_e32 v97, 0xffff0000, v214
	v_mul_f32_e32 v20, v92, v15
	v_add_f32_e32 v21, 1.0, v21
	v_rcp_f32_e32 v21, v21
	s_nop 0
	v_mul_f32_e32 v20, v228, v20
	v_mul_f32_e32 v20, v20, v30
	v_and_b32_e32 v18, 0xffff0000, v212
	v_mul_f32_e32 v26, v21, v20
	v_mul_f32_e32 v21, 0xbfb8aa3b, v96
	v_exp_f32_e32 v21, v21
	v_mul_f32_e32 v20, v88, v15
	v_mul_f32_e32 v20, v224, v20
	v_mul_f32_e32 v20, v20, v96
	v_add_f32_e32 v21, 1.0, v21
	v_rcp_f32_e32 v21, v21
	v_lshlrev_b32_e32 v31, 16, v213
	v_mul_f32_e32 v22, 0xbfb8aa3b, v31
	v_exp_f32_e32 v22, v22
	v_mul_f32_e32 v20, v21, v20
	v_mul_f32_e32 v21, v93, v15
	v_mul_f32_e32 v21, v229, v21
	v_mul_f32_e32 v21, v21, v18
	v_mul_f32_e32 v18, 0xbfb8aa3b, v18
	v_exp_f32_e32 v18, v18
	v_add_f32_e32 v22, 1.0, v22
	v_rcp_f32_e32 v22, v22
	v_and_b32_e32 v19, 0xffff0000, v213
	v_add_f32_e32 v18, 1.0, v18
	v_rcp_f32_e32 v18, v18
	s_nop 0
	v_mul_f32_e32 v27, v18, v21
	v_mul_f32_e32 v21, 0xbfb8aa3b, v97
	v_exp_f32_e32 v21, v21
	v_mul_f32_e32 v18, v89, v15
	v_mul_f32_e32 v18, v225, v18
	v_mul_f32_e32 v18, v18, v97
	v_add_f32_e32 v21, 1.0, v21
	v_rcp_f32_e32 v21, v21
	v_mul_f32_e32 v23, 0xbfb8aa3b, v99
	v_exp_f32_e32 v23, v23
	v_mul_f32_e32 v21, v21, v18
	v_mul_f32_e32 v18, v94, v15
	v_mul_f32_e32 v18, v230, v18
	v_mul_f32_e32 v18, v18, v31
	v_mul_f32_e32 v28, v22, v18
	v_mul_f32_e32 v22, 0xbfb8aa3b, v98
	v_exp_f32_e32 v22, v22
	v_mul_f32_e32 v18, v90, v15
	v_mul_f32_e32 v18, v226, v18
	v_mul_f32_e32 v18, v18, v98
	v_add_f32_e32 v22, 1.0, v22
	v_rcp_f32_e32 v22, v22
	v_add_f32_e32 v23, 1.0, v23
	v_rcp_f32_e32 v23, v23
	v_mul_f32_e32 v22, v22, v18
	v_mul_f32_e32 v18, v95, v15
	v_mul_f32_e32 v18, v231, v18
	v_mul_f32_e32 v18, v18, v19
	v_mul_f32_e32 v19, 0xbfb8aa3b, v19
	v_exp_f32_e32 v19, v19
	s_nop 0
	v_add_f32_e32 v19, 1.0, v19
	v_rcp_f32_e32 v19, v19
	s_nop 0
	v_mul_f32_e32 v19, v19, v18
	v_mul_f32_e32 v18, v91, v15
	v_mul_f32_e32 v18, v227, v18
	v_mul_f32_e32 v18, v18, v99
	v_mul_f32_e32 v23, v23, v18
	v_mov_b32_e32 v18, 0
	v_cvt_pk_fp8_f32 v18, v26, v27
	v_cvt_pk_fp8_f32 v18, v28, v19 op_sel:[0,0,1]
	v_mov_b32_e32 v19, 0
	v_cvt_pk_fp8_f32 v19, v20, v21
	v_cvt_pk_fp8_f32 v19, v22, v23 op_sel:[0,0,1]
	global_store_dwordx2 v[16:17], v[18:19], off
	s_nop 0
	s_nop 0
	s_nop 0
	s_nop 0
	s_waitcnt vmcnt(3)
	v_lshlrev_b32_e32 v30, 16, v216
	v_lshlrev_b32_e32 v90, 16, v219
	v_and_b32_e32 v91, 0xffff0000, v219
	v_mul_f32_e32 v21, 0xbfb8aa3b, v30
	v_exp_f32_e32 v21, v21
	v_lshlrev_b32_e32 v88, 16, v218
	v_and_b32_e32 v89, 0xffff0000, v218
	v_mul_f32_e32 v20, v84, v15
	v_add_f32_e32 v21, 1.0, v21
	v_rcp_f32_e32 v21, v21
	s_nop 0
	v_mul_f32_e32 v20, v20, v236
	v_mul_f32_e32 v20, v20, v30
	v_and_b32_e32 v18, 0xffff0000, v216
	v_mul_f32_e32 v26, v20, v21
	v_mul_f32_e32 v21, 0xbfb8aa3b, v88
	v_exp_f32_e32 v21, v21
	v_mul_f32_e32 v20, v80, v15
	v_mul_f32_e32 v20, v20, v232
	v_mul_f32_e32 v20, v20, v88
	v_add_f32_e32 v21, 1.0, v21
	v_rcp_f32_e32 v21, v21
	v_lshlrev_b32_e32 v31, 16, v217
	v_mul_f32_e32 v22, 0xbfb8aa3b, v31
	v_exp_f32_e32 v22, v22
	v_mul_f32_e32 v20, v20, v21
	v_mul_f32_e32 v21, v85, v15
	v_mul_f32_e32 v21, v21, v237
	v_mul_f32_e32 v21, v21, v18
	v_mul_f32_e32 v18, 0xbfb8aa3b, v18
	v_exp_f32_e32 v18, v18
	v_add_f32_e32 v22, 1.0, v22
	v_rcp_f32_e32 v22, v22
	v_and_b32_e32 v19, 0xffff0000, v217
	v_add_f32_e32 v18, 1.0, v18
	v_rcp_f32_e32 v18, v18
	s_nop 0
	v_mul_f32_e32 v27, v21, v18
	v_mul_f32_e32 v21, 0xbfb8aa3b, v89
	v_exp_f32_e32 v21, v21
	v_mul_f32_e32 v18, v81, v15
	v_mul_f32_e32 v18, v18, v233
	v_mul_f32_e32 v18, v18, v89
	v_add_f32_e32 v21, 1.0, v21
	v_rcp_f32_e32 v21, v21
	v_mul_f32_e32 v23, 0xbfb8aa3b, v91
	v_exp_f32_e32 v23, v23
	v_mul_f32_e32 v21, v18, v21
	v_mul_f32_e32 v18, v86, v15
	v_mul_f32_e32 v18, v18, v238
	v_mul_f32_e32 v18, v18, v31
	v_mul_f32_e32 v28, v18, v22
	v_mul_f32_e32 v22, 0xbfb8aa3b, v90
	v_exp_f32_e32 v22, v22
	v_mul_f32_e32 v18, v82, v15
	v_mul_f32_e32 v18, v18, v234
	v_mul_f32_e32 v18, v18, v90
	v_add_f32_e32 v22, 1.0, v22
	v_rcp_f32_e32 v22, v22
	v_add_f32_e32 v23, 1.0, v23
	v_rcp_f32_e32 v23, v23
	v_mul_f32_e32 v22, v18, v22
	v_mul_f32_e32 v18, v87, v15
	v_mul_f32_e32 v18, v18, v239
	v_mul_f32_e32 v18, v18, v19
	v_mul_f32_e32 v19, 0xbfb8aa3b, v19
	v_exp_f32_e32 v19, v19
	s_nop 0
	v_add_f32_e32 v19, 1.0, v19
	v_rcp_f32_e32 v19, v19
	s_nop 0
	v_mul_f32_e32 v19, v18, v19
	v_mul_f32_e32 v18, v83, v15
	v_mul_f32_e32 v18, v18, v235
	v_mul_f32_e32 v18, v18, v91
	v_mul_f32_e32 v23, v18, v23
	v_mov_b32_e32 v18, 0
	v_cvt_pk_fp8_f32 v18, v26, v27
	v_cvt_pk_fp8_f32 v18, v28, v19 op_sel:[0,0,1]
	v_mov_b32_e32 v19, 0
	v_cvt_pk_fp8_f32 v19, v20, v21
	v_cvt_pk_fp8_f32 v19, v22, v23 op_sel:[0,0,1]
	global_store_dwordx2 v[16:17], v[18:19], off offset:128
	s_nop 0
	s_nop 0
	s_nop 0
	s_nop 0
	s_waitcnt vmcnt(3)
	v_lshlrev_b32_e32 v30, 16, v174
	v_lshlrev_b32_e32 v82, 16, v177
	v_and_b32_e32 v83, 0xffff0000, v177
	v_mul_f32_e32 v21, 0xbfb8aa3b, v30
	v_exp_f32_e32 v21, v21
	v_lshlrev_b32_e32 v80, 16, v176
	v_and_b32_e32 v81, 0xffff0000, v176
	v_mul_f32_e32 v20, v76, v15
	v_add_f32_e32 v21, 1.0, v21
	v_rcp_f32_e32 v21, v21
	s_nop 0
	v_mul_f32_e32 v20, v20, v244
	v_mul_f32_e32 v20, v20, v30
	v_and_b32_e32 v18, 0xffff0000, v174
	v_mul_f32_e32 v26, v20, v21
	v_mul_f32_e32 v21, 0xbfb8aa3b, v80
	v_exp_f32_e32 v21, v21
	v_mul_f32_e32 v20, v72, v15
	v_mul_f32_e32 v20, v20, v240
	v_mul_f32_e32 v20, v20, v80
	v_add_f32_e32 v21, 1.0, v21
	v_rcp_f32_e32 v21, v21
	v_lshlrev_b32_e32 v31, 16, v175
	v_mul_f32_e32 v22, 0xbfb8aa3b, v31
	v_exp_f32_e32 v22, v22
	v_mul_f32_e32 v20, v20, v21
	v_mul_f32_e32 v21, v77, v15
	v_mul_f32_e32 v21, v21, v245
	v_mul_f32_e32 v21, v21, v18
	v_mul_f32_e32 v18, 0xbfb8aa3b, v18
	v_exp_f32_e32 v18, v18
	v_add_f32_e32 v22, 1.0, v22
	v_rcp_f32_e32 v22, v22
	v_and_b32_e32 v19, 0xffff0000, v175
	v_add_f32_e32 v18, 1.0, v18
	v_rcp_f32_e32 v18, v18
	s_nop 0
	v_mul_f32_e32 v27, v21, v18
	v_mul_f32_e32 v21, 0xbfb8aa3b, v81
	v_exp_f32_e32 v21, v21
	v_mul_f32_e32 v18, v73, v15
	v_mul_f32_e32 v18, v18, v241
	v_mul_f32_e32 v18, v18, v81
	v_add_f32_e32 v21, 1.0, v21
	v_rcp_f32_e32 v21, v21
	v_mul_f32_e32 v23, 0xbfb8aa3b, v83
	v_exp_f32_e32 v23, v23
	v_mul_f32_e32 v21, v18, v21
	v_mul_f32_e32 v18, v78, v15
	v_mul_f32_e32 v18, v18, v246
	v_mul_f32_e32 v18, v18, v31
	v_mul_f32_e32 v28, v18, v22
	v_mul_f32_e32 v22, 0xbfb8aa3b, v82
	v_exp_f32_e32 v22, v22
	v_mul_f32_e32 v18, v74, v15
	v_mul_f32_e32 v18, v18, v242
	v_mul_f32_e32 v18, v18, v82
	v_add_f32_e32 v22, 1.0, v22
	v_rcp_f32_e32 v22, v22
	v_add_f32_e32 v23, 1.0, v23
	v_rcp_f32_e32 v23, v23
	v_mul_f32_e32 v22, v18, v22
	v_mul_f32_e32 v18, v79, v15
	v_mul_f32_e32 v18, v18, v247
	v_mul_f32_e32 v18, v18, v19
	v_mul_f32_e32 v19, 0xbfb8aa3b, v19
	v_exp_f32_e32 v19, v19
	s_nop 0
	v_add_f32_e32 v19, 1.0, v19
	v_rcp_f32_e32 v19, v19
	s_nop 0
	v_mul_f32_e32 v19, v18, v19
	v_mul_f32_e32 v18, v75, v15
	v_mul_f32_e32 v18, v18, v243
	v_mul_f32_e32 v18, v18, v83
	v_mul_f32_e32 v23, v18, v23
	v_mov_b32_e32 v18, 0
	v_cvt_pk_fp8_f32 v18, v26, v27
	v_cvt_pk_fp8_f32 v18, v28, v19 op_sel:[0,0,1]
	v_mov_b32_e32 v19, 0
	v_cvt_pk_fp8_f32 v19, v20, v21
	v_cvt_pk_fp8_f32 v19, v22, v23 op_sel:[0,0,1]
	global_store_dwordx2 v[16:17], v[18:19], off offset:256
	s_nop 0
	s_nop 0
	s_nop 0
	s_nop 0
	s_waitcnt vmcnt(3)
	v_lshlrev_b32_e32 v6, 16, v178
	v_lshlrev_b32_e32 v30, 16, v180
	s_nop 0
	v_mul_f32_e32 v26, v68, v208
	v_mul_f32_e32 v26, v26, v6
	v_mul_f32_e32 v6, 0xbfb8aa3b, v6
	v_exp_f32_e32 v6, v6
	v_and_b32_e32 v7, 0xffff0000, v178
	v_and_b32_e32 v20, 0xffff0000, v180
	v_lshlrev_b32_e32 v18, 16, v179
	v_add_f32_e32 v6, 1.0, v6
	v_rcp_f32_e32 v6, v6
	v_lshlrev_b32_e32 v31, 16, v181
	v_and_b32_e32 v19, 0xffff0000, v179
	v_and_b32_e32 v21, 0xffff0000, v181
	v_mul_f32_e32 v26, v26, v6
	v_mul_f32_e32 v6, v64, v15
	v_mul_f32_e32 v6, v6, v204
	v_mul_f32_e32 v22, 0xbfb8aa3b, v30
	v_exp_f32_e32 v22, v22
	v_mul_f32_e32 v6, v6, v30
	v_add_f32_e32 v22, 1.0, v22
	v_rcp_f32_e32 v22, v22
	s_nop 0
	v_mul_f32_e32 v22, v6, v22
	v_mul_f32_e32 v6, v69, v15
	v_mul_f32_e32 v6, v6, v209
	v_mul_f32_e32 v6, v6, v7
	v_mul_f32_e32 v7, 0xbfb8aa3b, v7
	v_exp_f32_e32 v7, v7
	s_nop 0
	v_add_f32_e32 v7, 1.0, v7
	v_rcp_f32_e32 v7, v7
	s_nop 0
	v_mul_f32_e32 v7, v6, v7
	v_mul_f32_e32 v6, v65, v15
	v_mul_f32_e32 v6, v6, v205
	v_mul_f32_e32 v6, v6, v20
	v_mul_f32_e32 v20, 0xbfb8aa3b, v20
	v_exp_f32_e32 v20, v20
	v_mul_f32_e32 v23, 0xbfb8aa3b, v31
	v_exp_f32_e32 v23, v23
	v_add_f32_e32 v20, 1.0, v20
	v_rcp_f32_e32 v20, v20
	v_add_f32_e32 v23, 1.0, v23
	v_rcp_f32_e32 v23, v23
	v_mul_f32_e32 v20, v6, v20
	v_mul_f32_e32 v6, v70, v15
	v_mul_f32_e32 v6, v6, v210
	v_mul_f32_e32 v6, v6, v18
	v_mul_f32_e32 v18, 0xbfb8aa3b, v18
	v_exp_f32_e32 v18, v18
	s_nop 0
	v_add_f32_e32 v18, 1.0, v18
	v_rcp_f32_e32 v18, v18
	s_nop 0
	v_mul_f32_e32 v18, v6, v18
	v_mul_f32_e32 v6, v66, v15
	v_mul_f32_e32 v6, v6, v206
	v_mul_f32_e32 v6, v6, v31
	v_mul_f32_e32 v23, v6, v23
	v_mul_f32_e32 v6, v71, v15
	v_mul_f32_e32 v6, v6, v211
	v_mul_f32_e32 v6, v6, v19
	v_mul_f32_e32 v19, 0xbfb8aa3b, v19
	v_exp_f32_e32 v19, v19
	s_nop 0
	v_add_f32_e32 v19, 1.0, v19
	v_rcp_f32_e32 v19, v19
	s_nop 0
	v_mul_f32_e32 v19, v6, v19
	v_mul_f32_e32 v6, v67, v15
	v_mul_f32_e32 v15, 0xbfb8aa3b, v21
	v_exp_f32_e32 v15, v15
	v_mul_f32_e32 v6, v6, v207
	v_mul_f32_e32 v6, v6, v21
	v_add_f32_e32 v15, 1.0, v15
	v_rcp_f32_e32 v15, v15
	s_nop 0
	v_mul_f32_e32 v15, v6, v15
	v_mov_b32_e32 v6, 0
	v_cvt_pk_fp8_f32 v6, v26, v7
	v_mov_b32_e32 v7, 0
	v_cvt_pk_fp8_f32 v7, v22, v20
	v_cvt_pk_fp8_f32 v6, v18, v19 op_sel:[0,0,1]
	v_cvt_pk_fp8_f32 v7, v23, v15 op_sel:[0,0,1]
	global_store_dwordx2 v[16:17], v[6:7], off offset:384
	v_or_b32_e32 v6, 48, v14
	v_lshl_add_u32 v7, v6, 4, s0
	ds_read_b128 v[14:17], v7
	s_mov_b64 s[0:1], 0
	s_waitcnt lgkmcnt(0)
	v_mov_b32_e32 v18, v15
	v_mov_b32_e32 v19, v16
	v_mov_b32_e32 v15, v17
	v_pk_add_f32 v[14:15], v[18:19], v[14:15]
	s_nop 0
	v_add_f32_e32 v7, v14, v15
	v_fmamk_f32 v7, v7, 0x3b000000, v189
	v_rsq_f32_e32 v16, v7
	v_ashrrev_i32_e32 v7, 31, v6
	v_lshl_add_u64 v[14:15], s[20:21], 0, v[6:7]
	v_lshlrev_b64 v[6:7], 12, v[14:15]
	v_lshlrev_b64 v[14:15], 13, v[14:15]
	v_lshl_add_u64 v[18:19], s[66:67], 0, v[14:15]
	v_lshl_add_u64 v[14:15], s[34:35], 0, v[6:7]
	v_lshl_add_u64 v[6:7], v[18:19], 0, v[10:11]
	global_load_dwordx4 v[212:215], v[6:7], off nt
	global_load_dwordx4 v[216:219], v[6:7], off offset:256 nt
	global_load_dwordx4 v[174:177], v[6:7], off offset:512 nt
	global_load_dwordx4 v[178:181], v[6:7], off offset:768 nt
	s_nop 0
	s_nop 0
	v_lshl_add_u64 v[8:9], v[14:15], 0, v[8:9]
	s_waitcnt vmcnt(3)
	v_lshlrev_b32_e32 v10, 16, v212
	v_and_b32_e32 v11, 0xffff0000, v212
	v_lshlrev_b32_e32 v17, 16, v213
	v_and_b32_e32 v18, 0xffff0000, v213
	v_lshlrev_b32_e32 v12, 16, v214
	v_and_b32_e32 v13, 0xffff0000, v214
	v_lshlrev_b32_e32 v19, 16, v215
	v_and_b32_e32 v20, 0xffff0000, v215
	v_mul_f32_e32 v21, v60, v16
	s_nop 0
	v_mul_f32_e32 v21, v228, v21
	v_mul_f32_e32 v21, v21, v10
	v_mul_f32_e32 v10, 0xbfb8aa3b, v10
	v_exp_f32_e32 v10, v10
	s_nop 0
	v_add_f32_e32 v10, 1.0, v10
	v_rcp_f32_e32 v10, v10
	s_nop 0
	v_mul_f32_e32 v21, v10, v21
	v_mul_f32_e32 v10, v56, v16
	v_mul_f32_e32 v10, v224, v10
	v_mul_f32_e32 v10, v10, v12
	v_mul_f32_e32 v12, 0xbfb8aa3b, v12
	v_exp_f32_e32 v12, v12
	s_nop 0
	v_add_f32_e32 v12, 1.0, v12
	v_rcp_f32_e32 v12, v12
	s_nop 0
	v_mul_f32_e32 v12, v12, v10
	v_mul_f32_e32 v10, v61, v16
	v_mul_f32_e32 v10, v229, v10
	v_mul_f32_e32 v10, v10, v11
	v_mul_f32_e32 v11, 0xbfb8aa3b, v11
	v_exp_f32_e32 v11, v11
	s_nop 0
	v_add_f32_e32 v11, 1.0, v11
	v_rcp_f32_e32 v11, v11
	s_nop 0
	v_mul_f32_e32 v11, v11, v10
	v_mul_f32_e32 v10, v57, v16
	v_mul_f32_e32 v10, v225, v10
	v_mul_f32_e32 v10, v10, v13
	v_mul_f32_e32 v13, 0xbfb8aa3b, v13
	v_exp_f32_e32 v13, v13
	s_nop 0
	v_add_f32_e32 v13, 1.0, v13
	v_rcp_f32_e32 v13, v13
	s_nop 0
	v_mul_f32_e32 v13, v13, v10
	v_mul_f32_e32 v10, v62, v16
	v_mul_f32_e32 v10, v230, v10
	v_mul_f32_e32 v10, v10, v17
	v_mul_f32_e32 v17, 0xbfb8aa3b, v17
	v_exp_f32_e32 v17, v17
	s_nop 0
	v_add_f32_e32 v17, 1.0, v17
	v_rcp_f32_e32 v17, v17
	s_nop 0
	v_mul_f32_e32 v22, v17, v10
	v_mul_f32_e32 v17, 0xbfb8aa3b, v19
	v_exp_f32_e32 v17, v17
	v_mul_f32_e32 v10, v58, v16
	v_mul_f32_e32 v10, v226, v10
	v_mul_f32_e32 v10, v10, v19
	v_add_f32_e32 v17, 1.0, v17
	v_rcp_f32_e32 v17, v17
	s_nop 0
	v_mul_f32_e32 v17, v17, v10
	v_mul_f32_e32 v10, v63, v16
	v_mul_f32_e32 v10, v231, v10
	v_mul_f32_e32 v10, v10, v18
	v_mul_f32_e32 v18, 0xbfb8aa3b, v18
	v_exp_f32_e32 v18, v18
	s_nop 0
	v_add_f32_e32 v18, 1.0, v18
	v_rcp_f32_e32 v18, v18
	s_nop 0
	v_mul_f32_e32 v19, v18, v10
	v_mul_f32_e32 v18, 0xbfb8aa3b, v20
	v_exp_f32_e32 v18, v18
	v_mul_f32_e32 v10, v59, v16
	v_mul_f32_e32 v10, v227, v10
	v_mul_f32_e32 v10, v10, v20
	v_add_f32_e32 v18, 1.0, v18
	v_rcp_f32_e32 v18, v18
	s_nop 0
	v_mul_f32_e32 v18, v18, v10
	v_mov_b32_e32 v10, 0
	v_cvt_pk_fp8_f32 v10, v21, v11
	v_mov_b32_e32 v11, 0
	v_cvt_pk_fp8_f32 v11, v12, v13
	v_cvt_pk_fp8_f32 v10, v22, v19 op_sel:[0,0,1]
	v_cvt_pk_fp8_f32 v11, v17, v18 op_sel:[0,0,1]
	v_mul_f32_e32 v17, v52, v16
	global_store_dwordx2 v[8:9], v[10:11], off
	s_nop 0
	s_nop 0
	s_nop 0
	s_nop 0
	s_waitcnt vmcnt(3)
	v_lshlrev_b32_e32 v0, 16, v216
	v_and_b32_e32 v1, 0xffff0000, v216
	s_nop 0
	v_mul_f32_e32 v17, v17, v236
	v_mul_f32_e32 v17, v17, v0
	v_mul_f32_e32 v0, 0xbfb8aa3b, v0
	v_exp_f32_e32 v0, v0
	v_lshlrev_b32_e32 v10, 16, v218
	v_lshlrev_b32_e32 v14, 16, v217
	v_and_b32_e32 v15, 0xffff0000, v217
	v_add_f32_e32 v0, 1.0, v0
	v_rcp_f32_e32 v0, v0
	v_and_b32_e32 v11, 0xffff0000, v218
	v_lshlrev_b32_e32 v12, 16, v219
	v_and_b32_e32 v13, 0xffff0000, v219
	v_mul_f32_e32 v17, v17, v0
	v_mul_f32_e32 v0, v48, v16
	v_mul_f32_e32 v0, v0, v232
	v_mul_f32_e32 v0, v0, v10
	v_mul_f32_e32 v10, 0xbfb8aa3b, v10
	v_exp_f32_e32 v10, v10
	s_nop 0
	v_add_f32_e32 v10, 1.0, v10
	v_rcp_f32_e32 v10, v10
	s_nop 0
	v_mul_f32_e32 v10, v0, v10
	v_mul_f32_e32 v0, v53, v16
	v_mul_f32_e32 v0, v0, v237
	v_mul_f32_e32 v0, v0, v1
	v_mul_f32_e32 v1, 0xbfb8aa3b, v1
	v_exp_f32_e32 v1, v1
	s_nop 0
	v_add_f32_e32 v1, 1.0, v1
	v_rcp_f32_e32 v1, v1
	s_nop 0
	v_mul_f32_e32 v1, v0, v1
	v_mul_f32_e32 v0, v49, v16
	v_mul_f32_e32 v0, v0, v233
	v_mul_f32_e32 v0, v0, v11
	v_mul_f32_e32 v11, 0xbfb8aa3b, v11
	v_exp_f32_e32 v11, v11
	s_nop 0
	v_add_f32_e32 v11, 1.0, v11
	v_rcp_f32_e32 v11, v11
	s_nop 0
	v_mul_f32_e32 v11, v0, v11
	v_mul_f32_e32 v0, v54, v16
	v_mul_f32_e32 v0, v0, v238
	v_mul_f32_e32 v0, v0, v14
	v_mul_f32_e32 v14, 0xbfb8aa3b, v14
	v_exp_f32_e32 v14, v14
	s_nop 0
	v_add_f32_e32 v14, 1.0, v14
	v_rcp_f32_e32 v14, v14
	s_nop 0
	v_mul_f32_e32 v14, v0, v14
	v_mul_f32_e32 v0, v50, v16
	v_mul_f32_e32 v0, v0, v234
	v_mul_f32_e32 v0, v0, v12
	v_mul_f32_e32 v12, 0xbfb8aa3b, v12
	v_exp_f32_e32 v12, v12
	s_nop 0
	v_add_f32_e32 v12, 1.0, v12
	v_rcp_f32_e32 v12, v12
	s_nop 0
	v_mul_f32_e32 v12, v0, v12
	v_mul_f32_e32 v0, v55, v16
	v_mul_f32_e32 v0, v0, v239
	v_mul_f32_e32 v0, v0, v15
	v_mul_f32_e32 v15, 0xbfb8aa3b, v15
	v_exp_f32_e32 v15, v15
	s_nop 0
	v_add_f32_e32 v15, 1.0, v15
	v_rcp_f32_e32 v15, v15
	s_nop 0
	v_mul_f32_e32 v15, v0, v15
	v_mul_f32_e32 v0, v51, v16
	v_mul_f32_e32 v0, v0, v235
	v_mul_f32_e32 v0, v0, v13
	v_mul_f32_e32 v13, 0xbfb8aa3b, v13
	v_exp_f32_e32 v13, v13
	s_nop 0
	v_add_f32_e32 v13, 1.0, v13
	v_rcp_f32_e32 v13, v13
	s_nop 0
	v_mul_f32_e32 v13, v0, v13
	v_mov_b32_e32 v0, 0
	v_cvt_pk_fp8_f32 v0, v17, v1
	v_mov_b32_e32 v1, 0
	v_cvt_pk_fp8_f32 v1, v10, v11
	v_cvt_pk_fp8_f32 v0, v14, v15 op_sel:[0,0,1]
	v_mul_f32_e32 v14, v44, v16
	v_cvt_pk_fp8_f32 v1, v12, v13 op_sel:[0,0,1]
	global_store_dwordx2 v[8:9], v[0:1], off offset:128
	s_nop 0
	s_nop 0
	s_nop 0
	s_waitcnt vmcnt(3)
	v_lshlrev_b32_e32 v0, 16, v174
	v_lshlrev_b32_e32 v2, 16, v176
	s_nop 0
	v_mul_f32_e32 v14, v14, v244
	v_mul_f32_e32 v14, v14, v0
	v_mul_f32_e32 v0, 0xbfb8aa3b, v0
	v_exp_f32_e32 v0, v0
	v_and_b32_e32 v1, 0xffff0000, v174
	v_and_b32_e32 v3, 0xffff0000, v176
	v_lshlrev_b32_e32 v10, 16, v175
	v_add_f32_e32 v0, 1.0, v0
	v_rcp_f32_e32 v0, v0
	v_lshlrev_b32_e32 v12, 16, v177
	v_and_b32_e32 v11, 0xffff0000, v175
	v_and_b32_e32 v13, 0xffff0000, v177
	v_mul_f32_e32 v14, v14, v0
	v_mul_f32_e32 v0, v40, v16
	v_mul_f32_e32 v0, v0, v240
	v_mul_f32_e32 v0, v0, v2
	v_mul_f32_e32 v2, 0xbfb8aa3b, v2
	v_exp_f32_e32 v2, v2
	s_nop 0
	v_add_f32_e32 v2, 1.0, v2
	v_rcp_f32_e32 v2, v2
	s_nop 0
	v_mul_f32_e32 v2, v0, v2
	v_mul_f32_e32 v0, v45, v16
	v_mul_f32_e32 v0, v0, v245
	v_mul_f32_e32 v0, v0, v1
	v_mul_f32_e32 v1, 0xbfb8aa3b, v1
	v_exp_f32_e32 v1, v1
	s_nop 0
	v_add_f32_e32 v1, 1.0, v1
	v_rcp_f32_e32 v1, v1
	s_nop 0
	v_mul_f32_e32 v1, v0, v1
	v_mul_f32_e32 v0, v41, v16
	v_mul_f32_e32 v0, v0, v241
	v_mul_f32_e32 v0, v0, v3
	v_mul_f32_e32 v3, 0xbfb8aa3b, v3
	v_exp_f32_e32 v3, v3
	s_nop 0
	v_add_f32_e32 v3, 1.0, v3
	v_rcp_f32_e32 v3, v3
	s_nop 0
	v_mul_f32_e32 v3, v0, v3
	v_mul_f32_e32 v0, v46, v16
	v_mul_f32_e32 v0, v0, v246
	v_mul_f32_e32 v0, v0, v10
	v_mul_f32_e32 v10, 0xbfb8aa3b, v10
	v_exp_f32_e32 v10, v10
	s_nop 0
	v_add_f32_e32 v10, 1.0, v10
	v_rcp_f32_e32 v10, v10
	s_nop 0
	v_mul_f32_e32 v15, v0, v10
	v_mul_f32_e32 v10, 0xbfb8aa3b, v12
	v_exp_f32_e32 v10, v10
	v_mul_f32_e32 v0, v42, v16
	v_mul_f32_e32 v0, v0, v242
	v_mul_f32_e32 v0, v0, v12
	v_add_f32_e32 v10, 1.0, v10
	v_rcp_f32_e32 v10, v10
	s_nop 0
	v_mul_f32_e32 v10, v0, v10
	v_mul_f32_e32 v0, v47, v16
	v_mul_f32_e32 v0, v0, v247
	v_mul_f32_e32 v0, v0, v11
	v_mul_f32_e32 v11, 0xbfb8aa3b, v11
	v_exp_f32_e32 v11, v11
	s_nop 0
	v_add_f32_e32 v11, 1.0, v11
	v_rcp_f32_e32 v11, v11
	s_nop 0
	v_mul_f32_e32 v12, v0, v11
	v_mul_f32_e32 v11, 0xbfb8aa3b, v13
	v_exp_f32_e32 v11, v11
	v_mul_f32_e32 v0, v43, v16
	v_mul_f32_e32 v0, v0, v243
	v_mul_f32_e32 v0, v0, v13
	v_add_f32_e32 v11, 1.0, v11
	v_rcp_f32_e32 v11, v11
	s_nop 0
	v_mul_f32_e32 v11, v0, v11
	v_mov_b32_e32 v0, 0
	v_cvt_pk_fp8_f32 v0, v14, v1
	v_mov_b32_e32 v1, 0
	v_cvt_pk_fp8_f32 v1, v2, v3
	v_cvt_pk_fp8_f32 v0, v15, v12 op_sel:[0,0,1]
	v_cvt_pk_fp8_f32 v1, v10, v11 op_sel:[0,0,1]
	global_store_dwordx2 v[8:9], v[0:1], off offset:256
	s_nop 0
	s_nop 0
	s_nop 0
	s_nop 0
	s_nop 0
	s_waitcnt vmcnt(3)
	v_lshlrev_b32_e32 v14, 16, v178
	v_lshlrev_b32_e32 v19, 16, v181
	v_and_b32_e32 v20, 0xffff0000, v181
	v_mul_f32_e32 v3, 0xbfb8aa3b, v14
	v_exp_f32_e32 v3, v3
	v_lshlrev_b32_e32 v17, 16, v180
	v_and_b32_e32 v18, 0xffff0000, v180
	v_mul_f32_e32 v2, v36, v16
	v_add_f32_e32 v3, 1.0, v3
	v_rcp_f32_e32 v3, v3
	s_nop 0
	v_mul_f32_e32 v2, v2, v208
	v_mul_f32_e32 v2, v2, v14
	v_and_b32_e32 v0, 0xffff0000, v178
	v_mul_f32_e32 v14, v2, v3
	v_mul_f32_e32 v3, 0xbfb8aa3b, v17
	v_exp_f32_e32 v3, v3
	v_mul_f32_e32 v2, v32, v16
	v_mul_f32_e32 v2, v2, v204
	v_mul_f32_e32 v2, v2, v17
	v_add_f32_e32 v3, 1.0, v3
	v_rcp_f32_e32 v3, v3
	v_lshlrev_b32_e32 v15, 16, v179
	v_mul_f32_e32 v4, 0xbfb8aa3b, v15
	v_exp_f32_e32 v4, v4
	v_mul_f32_e32 v2, v2, v3
	v_mul_f32_e32 v3, v37, v16
	v_mul_f32_e32 v3, v3, v209
	v_mul_f32_e32 v3, v3, v0
	v_mul_f32_e32 v0, 0xbfb8aa3b, v0
	v_exp_f32_e32 v0, v0
	v_add_f32_e32 v4, 1.0, v4
	v_rcp_f32_e32 v4, v4
	v_and_b32_e32 v1, 0xffff0000, v179
	v_add_f32_e32 v0, 1.0, v0
	v_rcp_f32_e32 v0, v0
	v_mul_f32_e32 v5, 0xbfb8aa3b, v20
	v_exp_f32_e32 v5, v5
	v_mul_f32_e32 v10, v3, v0
	v_mul_f32_e32 v3, 0xbfb8aa3b, v18
	v_exp_f32_e32 v3, v3
	v_mul_f32_e32 v0, v33, v16
	v_mul_f32_e32 v0, v0, v205
	v_mul_f32_e32 v0, v0, v18
	v_add_f32_e32 v3, 1.0, v3
	v_rcp_f32_e32 v3, v3
	v_add_f32_e32 v5, 1.0, v5
	v_rcp_f32_e32 v5, v5
	v_mul_f32_e32 v3, v0, v3
	v_mul_f32_e32 v0, v38, v16
	v_mul_f32_e32 v0, v0, v210
	v_mul_f32_e32 v0, v0, v15
	v_mul_f32_e32 v6, v0, v4
	v_mul_f32_e32 v4, 0xbfb8aa3b, v19
	v_exp_f32_e32 v4, v4
	v_mul_f32_e32 v0, v34, v16
	v_mul_f32_e32 v0, v0, v206
	v_mul_f32_e32 v0, v0, v19
	v_add_f32_e32 v4, 1.0, v4
	v_rcp_f32_e32 v4, v4
	s_nop 0
	v_mul_f32_e32 v4, v0, v4
	v_mul_f32_e32 v0, v39, v16
	v_mul_f32_e32 v0, v0, v211
	v_mul_f32_e32 v0, v0, v1
	v_mul_f32_e32 v1, 0xbfb8aa3b, v1
	v_exp_f32_e32 v1, v1
	s_nop 0
	v_add_f32_e32 v1, 1.0, v1
	v_rcp_f32_e32 v1, v1
	s_nop 0
	v_mul_f32_e32 v1, v0, v1
	v_mul_f32_e32 v0, v35, v16
	v_mul_f32_e32 v0, v0, v207
	v_mul_f32_e32 v0, v0, v20
	v_mul_f32_e32 v5, v0, v5
	v_mov_b32_e32 v0, 0
	v_cvt_pk_fp8_f32 v0, v14, v10
	v_cvt_pk_fp8_f32 v0, v6, v1 op_sel:[0,0,1]
	v_mov_b32_e32 v1, 0
	v_cvt_pk_fp8_f32 v1, v2, v3
	v_cvt_pk_fp8_f32 v1, v4, v5 op_sel:[0,0,1]
	global_store_dwordx2 v[8:9], v[0:1], off offset:384
	s_waitcnt vmcnt(0)
	s_barrier
	s_cbranch_vccnz .LBB0_592
